# v049 + conv31 LayerNorm wave sums: xor-1/2/4/8 butterfly steps via DPP moves instead of ds_bpermute round trips
# baseline (speedup 1.0000x reference)
.LBB0_346:
	s_sub_i32 s0, s4, 31
	s_ashr_i32 s1, s0, 31
	s_lshl_b64 s[0:1], s[0:1], 11
	s_waitcnt vmcnt(0)
	v_lshlrev_b32_e32 v178, 16, v33
	v_and_b32_e32 v179, 0xffff0000, v33
	v_lshlrev_b32_e32 v180, 16, v32
	v_and_b32_e32 v181, 0xffff0000, v32
	v_lshl_add_u64 v[32:33], v[110:111], 0, s[0:1]
	s_sub_i32 s0, s4, 30
	s_ashr_i32 s1, s0, 31
	s_lshl_b64 s[0:1], s[0:1], 11
	v_lshlrev_b32_e32 v174, 16, v35
	v_and_b32_e32 v175, 0xffff0000, v35
	v_lshlrev_b32_e32 v176, 16, v34
	v_and_b32_e32 v177, 0xffff0000, v34
	v_lshl_add_u64 v[34:35], v[110:111], 0, s[0:1]
	s_sub_i32 s0, s4, 29
	s_ashr_i32 s1, s0, 31
	s_lshl_b64 s[0:1], s[0:1], 11
	v_lshlrev_b32_e32 v170, 16, v37
	v_and_b32_e32 v171, 0xffff0000, v37
	v_lshlrev_b32_e32 v172, 16, v36
	v_and_b32_e32 v173, 0xffff0000, v36
	v_lshl_add_u64 v[36:37], v[110:111], 0, s[0:1]
	s_sub_i32 s0, s4, 28
	s_ashr_i32 s1, s0, 31
	s_lshl_b64 s[0:1], s[0:1], 11
	v_lshlrev_b32_e32 v166, 16, v39
	v_and_b32_e32 v167, 0xffff0000, v39
	v_lshlrev_b32_e32 v168, 16, v38
	v_and_b32_e32 v169, 0xffff0000, v38
	v_lshl_add_u64 v[38:39], v[110:111], 0, s[0:1]
	s_sub_i32 s0, s4, 27
	s_ashr_i32 s1, s0, 31
	s_lshl_b64 s[0:1], s[0:1], 11
	v_lshlrev_b32_e32 v160, 16, v41
	v_and_b32_e32 v161, 0xffff0000, v41
	v_lshlrev_b32_e32 v164, 16, v40
	v_and_b32_e32 v165, 0xffff0000, v40
	v_lshl_add_u64 v[40:41], v[110:111], 0, s[0:1]
	s_sub_i32 s0, s4, 26
	s_ashr_i32 s1, s0, 31
	s_lshl_b64 s[0:1], s[0:1], 11
	v_lshl_add_u64 v[42:43], v[110:111], 0, s[0:1]
	s_sub_i32 s0, s4, 25
	s_ashr_i32 s1, s0, 31
	s_lshl_b64 s[0:1], s[0:1], 11
	v_lshl_add_u64 v[44:45], v[110:111], 0, s[0:1]
	s_sub_i32 s0, s4, 24
	s_ashr_i32 s1, s0, 31
	s_lshl_b64 s[0:1], s[0:1], 11
	v_lshl_add_u64 v[120:121], v[110:111], 0, s[0:1]
	s_sub_i32 s0, s4, 23
	s_ashr_i32 s1, s0, 31
	s_lshl_b64 s[0:1], s[0:1], 11
	v_lshlrev_b32_e32 v182, 16, v31
	v_and_b32_e32 v183, 0xffff0000, v31
	global_load_dword v31, v[32:33], off
	global_load_dword v122, v[34:35], off
	global_load_dword v123, v[36:37], off
	global_load_dword v124, v[38:39], off
	global_load_dword v125, v[40:41], off
	global_load_dword v126, v[42:43], off
	global_load_dword v127, v[44:45], off
	global_load_dword v128, v[120:121], off
	v_lshl_add_u64 v[32:33], v[110:111], 0, s[0:1]
	s_sub_i32 s0, s4, 22
	s_ashr_i32 s1, s0, 31
	s_lshl_b64 s[0:1], s[0:1], 11
	v_lshl_add_u64 v[34:35], v[110:111], 0, s[0:1]
	s_sub_i32 s0, s4, 21
	s_ashr_i32 s1, s0, 31
	s_lshl_b64 s[0:1], s[0:1], 11
	v_lshl_add_u64 v[36:37], v[110:111], 0, s[0:1]
	s_sub_i32 s0, s4, 20
	s_ashr_i32 s1, s0, 31
	s_lshl_b64 s[0:1], s[0:1], 11
	v_lshl_add_u64 v[38:39], v[110:111], 0, s[0:1]
	s_sub_i32 s0, s4, 19
	s_ashr_i32 s1, s0, 31
	s_lshl_b64 s[0:1], s[0:1], 11
	v_lshl_add_u64 v[40:41], v[110:111], 0, s[0:1]
	s_sub_i32 s0, s4, 18
	s_ashr_i32 s1, s0, 31
	s_lshl_b64 s[0:1], s[0:1], 11
	v_lshl_add_u64 v[42:43], v[110:111], 0, s[0:1]
	s_sub_i32 s0, s4, 17
	s_ashr_i32 s1, s0, 31
	s_lshl_b64 s[0:1], s[0:1], 11
	v_lshl_add_u64 v[44:45], v[110:111], 0, s[0:1]
	s_add_i32 s0, s4, -16
	s_ashr_i32 s1, s0, 31
	s_lshl_b64 s[0:1], s[0:1], 11
	v_lshl_add_u64 v[120:121], v[110:111], 0, s[0:1]
	s_add_i32 s0, s4, -15
	s_ashr_i32 s1, s0, 31
	s_lshl_b64 s[0:1], s[0:1], 11
	global_load_dword v129, v[32:33], off
	global_load_dword v130, v[34:35], off
	global_load_dword v131, v[36:37], off
	global_load_dword v132, v[38:39], off
	global_load_dword v133, v[40:41], off
	global_load_dword v134, v[42:43], off
	global_load_dword v135, v[44:45], off
	global_load_dword v136, v[120:121], off
	v_lshl_add_u64 v[32:33], v[110:111], 0, s[0:1]
	s_add_i32 s0, s4, -14
	s_ashr_i32 s1, s0, 31
	s_lshl_b64 s[0:1], s[0:1], 11
	v_lshl_add_u64 v[34:35], v[110:111], 0, s[0:1]
	s_add_i32 s0, s4, -13
	s_ashr_i32 s1, s0, 31
	s_lshl_b64 s[0:1], s[0:1], 11
	v_lshl_add_u64 v[36:37], v[110:111], 0, s[0:1]
	s_add_i32 s0, s4, -12
	s_ashr_i32 s1, s0, 31
	s_lshl_b64 s[0:1], s[0:1], 11
	v_lshl_add_u64 v[38:39], v[110:111], 0, s[0:1]
	s_add_i32 s0, s4, -11
	s_ashr_i32 s1, s0, 31
	s_lshl_b64 s[0:1], s[0:1], 11
	v_lshl_add_u64 v[40:41], v[110:111], 0, s[0:1]
	s_add_i32 s0, s4, -10
	s_ashr_i32 s1, s0, 31
	s_lshl_b64 s[0:1], s[0:1], 11
	v_lshl_add_u64 v[42:43], v[110:111], 0, s[0:1]
	s_add_i32 s0, s4, -9
	s_ashr_i32 s1, s0, 31
	s_lshl_b64 s[0:1], s[0:1], 11
	v_lshl_add_u64 v[44:45], v[110:111], 0, s[0:1]
	s_add_i32 s0, s4, -8
	s_ashr_i32 s1, s0, 31
	s_lshl_b64 s[0:1], s[0:1], 11
	v_lshl_add_u64 v[120:121], v[110:111], 0, s[0:1]
	s_add_i32 s0, s4, -7
	s_ashr_i32 s1, s0, 31
	s_lshl_b64 s[0:1], s[0:1], 11
	global_load_dword v137, v[32:33], off
	global_load_dword v138, v[34:35], off
	global_load_dword v139, v[36:37], off
	global_load_dword v140, v[38:39], off
	global_load_dword v141, v[40:41], off
	global_load_dword v142, v[42:43], off
	global_load_dword v143, v[44:45], off
	global_load_dword v144, v[120:121], off
	v_lshl_add_u64 v[32:33], v[110:111], 0, s[0:1]
	s_add_i32 s0, s4, -6
	s_ashr_i32 s1, s0, 31
	s_lshl_b64 s[0:1], s[0:1], 11
	v_lshl_add_u64 v[34:35], v[110:111], 0, s[0:1]
	s_add_i32 s0, s4, -5
	s_ashr_i32 s1, s0, 31
	s_lshl_b64 s[0:1], s[0:1], 11
	v_lshl_add_u64 v[36:37], v[110:111], 0, s[0:1]
	s_add_i32 s0, s4, -4
	s_ashr_i32 s1, s0, 31
	s_lshl_b64 s[0:1], s[0:1], 11
	v_lshl_add_u64 v[38:39], v[110:111], 0, s[0:1]
	s_add_i32 s0, s4, -3
	s_ashr_i32 s1, s0, 31
	s_lshl_b64 s[0:1], s[0:1], 11
	global_load_dword v145, v[32:33], off
	global_load_dword v146, v[34:35], off
	global_load_dword v147, v[36:37], off
	global_load_dword v149, v[38:39], off
	v_lshl_add_u64 v[32:33], v[110:111], 0, s[0:1]
	s_add_i32 s0, s4, -2
	s_ashr_i32 s1, s0, 31
	s_lshl_b64 s[0:1], s[0:1], 11
	v_lshl_add_u64 v[34:35], v[110:111], 0, s[0:1]
	s_add_i32 s0, s4, -1
	s_ashr_i32 s1, s0, 31
	s_lshl_b64 s[0:1], s[0:1], 11
	v_lshl_add_u64 v[36:37], v[110:111], 0, s[0:1]
	global_load_dword v151, v[32:33], off
	global_load_dword v153, v[34:35], off
	global_load_dword v155, v[36:37], off
	v_lshlrev_b32_e32 v224, 16, v22
	v_and_b32_e32 v225, 0xffff0000, v22
	v_lshlrev_b32_e32 v222, 16, v24
	v_and_b32_e32 v223, 0xffff0000, v24
	v_pk_fma_f32 v[224:225], v[106:107], v[224:225], v[108:109]
	v_lshlrev_b32_e32 v220, 16, v23
	v_and_b32_e32 v221, 0xffff0000, v23
	v_pk_fma_f32 v[224:225], v[46:47], v[222:223], v[224:225]
	v_pk_fma_f32 v[222:223], v[106:107], v[222:223], v[108:109]
	v_lshlrev_b32_e32 v216, 16, v25
	v_and_b32_e32 v217, 0xffff0000, v25
	v_pk_fma_f32 v[224:225], v[48:49], v[220:221], v[224:225]
	v_pk_fma_f32 v[222:223], v[46:47], v[220:221], v[222:223]
	v_pk_fma_f32 v[220:221], v[106:107], v[220:221], v[108:109]
	v_lshlrev_b32_e32 v214, 16, v26
	v_and_b32_e32 v215, 0xffff0000, v26
	v_pk_fma_f32 v[224:225], v[50:51], v[216:217], v[224:225]
	v_pk_fma_f32 v[222:223], v[48:49], v[216:217], v[222:223]
	v_pk_fma_f32 v[220:221], v[46:47], v[216:217], v[220:221]
	v_pk_fma_f32 v[216:217], v[106:107], v[216:217], v[108:109]
	v_lshlrev_b32_e32 v212, 16, v27
	v_and_b32_e32 v213, 0xffff0000, v27
	v_pk_fma_f32 v[224:225], v[52:53], v[214:215], v[224:225]
	v_pk_fma_f32 v[222:223], v[50:51], v[214:215], v[222:223]
	v_pk_fma_f32 v[220:221], v[48:49], v[214:215], v[220:221]
	v_pk_fma_f32 v[216:217], v[46:47], v[214:215], v[216:217]
	v_pk_fma_f32 v[214:215], v[106:107], v[214:215], v[108:109]
	v_lshlrev_b32_e32 v186, 16, v28
	v_and_b32_e32 v187, 0xffff0000, v28
	v_pk_fma_f32 v[224:225], v[54:55], v[212:213], v[224:225]
	v_pk_fma_f32 v[222:223], v[52:53], v[212:213], v[222:223]
	v_pk_fma_f32 v[220:221], v[50:51], v[212:213], v[220:221]
	v_pk_fma_f32 v[216:217], v[48:49], v[212:213], v[216:217]
	v_pk_fma_f32 v[214:215], v[46:47], v[212:213], v[214:215]
	v_pk_fma_f32 v[212:213], v[106:107], v[212:213], v[108:109]
	v_lshlrev_b32_e32 v184, 16, v29
	v_and_b32_e32 v185, 0xffff0000, v29
	v_pk_fma_f32 v[224:225], v[56:57], v[186:187], v[224:225]
	v_pk_fma_f32 v[222:223], v[54:55], v[186:187], v[222:223]
	v_pk_fma_f32 v[220:221], v[52:53], v[186:187], v[220:221]
	v_pk_fma_f32 v[216:217], v[50:51], v[186:187], v[216:217]
	v_pk_fma_f32 v[214:215], v[48:49], v[186:187], v[214:215]
	v_pk_fma_f32 v[212:213], v[46:47], v[186:187], v[212:213]
	v_pk_fma_f32 v[186:187], v[106:107], v[186:187], v[108:109]
	v_pk_fma_f32 v[224:225], v[58:59], v[184:185], v[224:225]
	v_pk_fma_f32 v[222:223], v[56:57], v[184:185], v[222:223]
	v_pk_fma_f32 v[220:221], v[54:55], v[184:185], v[220:221]
	v_pk_fma_f32 v[216:217], v[52:53], v[184:185], v[216:217]
	v_pk_fma_f32 v[214:215], v[50:51], v[184:185], v[214:215]
	v_pk_fma_f32 v[212:213], v[48:49], v[184:185], v[212:213]
	v_pk_fma_f32 v[186:187], v[46:47], v[184:185], v[186:187]
	v_pk_fma_f32 v[184:185], v[106:107], v[184:185], v[108:109]
	v_pk_fma_f32 v[224:225], v[60:61], v[182:183], v[224:225]
	v_pk_fma_f32 v[222:223], v[58:59], v[182:183], v[222:223]
	v_pk_fma_f32 v[220:221], v[56:57], v[182:183], v[220:221]
	v_pk_fma_f32 v[216:217], v[54:55], v[182:183], v[216:217]
	v_pk_fma_f32 v[214:215], v[52:53], v[182:183], v[214:215]
	v_pk_fma_f32 v[212:213], v[50:51], v[182:183], v[212:213]
	v_pk_fma_f32 v[186:187], v[48:49], v[182:183], v[186:187]
	v_pk_fma_f32 v[184:185], v[46:47], v[182:183], v[184:185]
	v_pk_fma_f32 v[182:183], v[106:107], v[182:183], v[108:109]
	v_pk_fma_f32 v[224:225], v[62:63], v[180:181], v[224:225]
	v_pk_fma_f32 v[222:223], v[60:61], v[180:181], v[222:223]
	v_pk_fma_f32 v[220:221], v[58:59], v[180:181], v[220:221]
	v_pk_fma_f32 v[216:217], v[56:57], v[180:181], v[216:217]
	v_pk_fma_f32 v[214:215], v[54:55], v[180:181], v[214:215]
	v_pk_fma_f32 v[212:213], v[52:53], v[180:181], v[212:213]
	v_pk_fma_f32 v[186:187], v[50:51], v[180:181], v[186:187]
	v_pk_fma_f32 v[184:185], v[48:49], v[180:181], v[184:185]
	v_pk_fma_f32 v[182:183], v[46:47], v[180:181], v[182:183]
	v_pk_fma_f32 v[180:181], v[106:107], v[180:181], v[108:109]
	v_pk_fma_f32 v[224:225], v[64:65], v[178:179], v[224:225]
	v_pk_fma_f32 v[222:223], v[62:63], v[178:179], v[222:223]
	v_pk_fma_f32 v[220:221], v[60:61], v[178:179], v[220:221]
	v_pk_fma_f32 v[216:217], v[58:59], v[178:179], v[216:217]
	v_pk_fma_f32 v[214:215], v[56:57], v[178:179], v[214:215]
	v_pk_fma_f32 v[212:213], v[54:55], v[178:179], v[212:213]
	v_pk_fma_f32 v[186:187], v[52:53], v[178:179], v[186:187]
	v_pk_fma_f32 v[184:185], v[50:51], v[178:179], v[184:185]
	v_pk_fma_f32 v[182:183], v[48:49], v[178:179], v[182:183]
	v_pk_fma_f32 v[180:181], v[46:47], v[178:179], v[180:181]
	v_pk_fma_f32 v[178:179], v[106:107], v[178:179], v[108:109]
	v_pk_fma_f32 v[224:225], v[66:67], v[176:177], v[224:225]
	v_pk_fma_f32 v[222:223], v[64:65], v[176:177], v[222:223]
	v_pk_fma_f32 v[220:221], v[62:63], v[176:177], v[220:221]
	v_pk_fma_f32 v[216:217], v[60:61], v[176:177], v[216:217]
	v_pk_fma_f32 v[214:215], v[58:59], v[176:177], v[214:215]
	v_pk_fma_f32 v[212:213], v[56:57], v[176:177], v[212:213]
	v_pk_fma_f32 v[186:187], v[54:55], v[176:177], v[186:187]
	v_pk_fma_f32 v[184:185], v[52:53], v[176:177], v[184:185]
	v_pk_fma_f32 v[182:183], v[50:51], v[176:177], v[182:183]
	v_pk_fma_f32 v[180:181], v[48:49], v[176:177], v[180:181]
	v_pk_fma_f32 v[178:179], v[46:47], v[176:177], v[178:179]
	v_pk_fma_f32 v[176:177], v[106:107], v[176:177], v[108:109]
	v_pk_fma_f32 v[224:225], v[68:69], v[174:175], v[224:225]
	v_pk_fma_f32 v[222:223], v[66:67], v[174:175], v[222:223]
	v_pk_fma_f32 v[220:221], v[64:65], v[174:175], v[220:221]
	v_pk_fma_f32 v[216:217], v[62:63], v[174:175], v[216:217]
	v_pk_fma_f32 v[214:215], v[60:61], v[174:175], v[214:215]
	v_pk_fma_f32 v[212:213], v[58:59], v[174:175], v[212:213]
	v_pk_fma_f32 v[186:187], v[56:57], v[174:175], v[186:187]
	v_pk_fma_f32 v[184:185], v[54:55], v[174:175], v[184:185]
	v_pk_fma_f32 v[182:183], v[52:53], v[174:175], v[182:183]
	v_pk_fma_f32 v[180:181], v[50:51], v[174:175], v[180:181]
	v_pk_fma_f32 v[178:179], v[48:49], v[174:175], v[178:179]
	v_pk_fma_f32 v[176:177], v[46:47], v[174:175], v[176:177]
	v_pk_fma_f32 v[174:175], v[106:107], v[174:175], v[108:109]
	v_pk_fma_f32 v[224:225], v[70:71], v[172:173], v[224:225]
	v_pk_fma_f32 v[222:223], v[68:69], v[172:173], v[222:223]
	v_pk_fma_f32 v[220:221], v[66:67], v[172:173], v[220:221]
	v_pk_fma_f32 v[216:217], v[64:65], v[172:173], v[216:217]
	v_pk_fma_f32 v[214:215], v[62:63], v[172:173], v[214:215]
	v_pk_fma_f32 v[212:213], v[60:61], v[172:173], v[212:213]
	v_pk_fma_f32 v[186:187], v[58:59], v[172:173], v[186:187]
	v_pk_fma_f32 v[184:185], v[56:57], v[172:173], v[184:185]
	v_pk_fma_f32 v[182:183], v[54:55], v[172:173], v[182:183]
	v_pk_fma_f32 v[180:181], v[52:53], v[172:173], v[180:181]
	v_pk_fma_f32 v[178:179], v[50:51], v[172:173], v[178:179]
	v_pk_fma_f32 v[176:177], v[48:49], v[172:173], v[176:177]
	v_pk_fma_f32 v[174:175], v[46:47], v[172:173], v[174:175]
	v_pk_fma_f32 v[172:173], v[106:107], v[172:173], v[108:109]
	v_pk_fma_f32 v[224:225], v[72:73], v[170:171], v[224:225]
	v_pk_fma_f32 v[222:223], v[70:71], v[170:171], v[222:223]
	v_pk_fma_f32 v[220:221], v[68:69], v[170:171], v[220:221]
	v_pk_fma_f32 v[216:217], v[66:67], v[170:171], v[216:217]
	v_pk_fma_f32 v[214:215], v[64:65], v[170:171], v[214:215]
	v_pk_fma_f32 v[212:213], v[62:63], v[170:171], v[212:213]
	v_pk_fma_f32 v[186:187], v[60:61], v[170:171], v[186:187]
	v_pk_fma_f32 v[184:185], v[58:59], v[170:171], v[184:185]
	v_pk_fma_f32 v[182:183], v[56:57], v[170:171], v[182:183]
	v_pk_fma_f32 v[180:181], v[54:55], v[170:171], v[180:181]
	v_pk_fma_f32 v[178:179], v[52:53], v[170:171], v[178:179]
	v_pk_fma_f32 v[176:177], v[50:51], v[170:171], v[176:177]
	v_pk_fma_f32 v[174:175], v[48:49], v[170:171], v[174:175]
	v_pk_fma_f32 v[172:173], v[46:47], v[170:171], v[172:173]
	v_pk_fma_f32 v[170:171], v[106:107], v[170:171], v[108:109]
	v_pk_fma_f32 v[224:225], v[74:75], v[168:169], v[224:225]
	v_pk_fma_f32 v[222:223], v[72:73], v[168:169], v[222:223]
	v_pk_fma_f32 v[220:221], v[70:71], v[168:169], v[220:221]
	v_pk_fma_f32 v[216:217], v[68:69], v[168:169], v[216:217]
	v_pk_fma_f32 v[214:215], v[66:67], v[168:169], v[214:215]
	v_pk_fma_f32 v[212:213], v[64:65], v[168:169], v[212:213]
	v_pk_fma_f32 v[186:187], v[62:63], v[168:169], v[186:187]
	v_pk_fma_f32 v[184:185], v[60:61], v[168:169], v[184:185]
	v_pk_fma_f32 v[182:183], v[58:59], v[168:169], v[182:183]
	v_pk_fma_f32 v[180:181], v[56:57], v[168:169], v[180:181]
	v_pk_fma_f32 v[178:179], v[54:55], v[168:169], v[178:179]
	v_pk_fma_f32 v[176:177], v[52:53], v[168:169], v[176:177]
	v_pk_fma_f32 v[174:175], v[50:51], v[168:169], v[174:175]
	v_pk_fma_f32 v[172:173], v[48:49], v[168:169], v[172:173]
	v_pk_fma_f32 v[170:171], v[46:47], v[168:169], v[170:171]
	v_pk_fma_f32 v[168:169], v[106:107], v[168:169], v[108:109]
	v_pk_fma_f32 v[224:225], v[76:77], v[166:167], v[224:225]
	v_pk_fma_f32 v[222:223], v[74:75], v[166:167], v[222:223]
	v_pk_fma_f32 v[220:221], v[72:73], v[166:167], v[220:221]
	v_pk_fma_f32 v[216:217], v[70:71], v[166:167], v[216:217]
	v_pk_fma_f32 v[214:215], v[68:69], v[166:167], v[214:215]
	v_pk_fma_f32 v[212:213], v[66:67], v[166:167], v[212:213]
	v_pk_fma_f32 v[186:187], v[64:65], v[166:167], v[186:187]
	v_pk_fma_f32 v[184:185], v[62:63], v[166:167], v[184:185]
	v_pk_fma_f32 v[182:183], v[60:61], v[166:167], v[182:183]
	v_pk_fma_f32 v[180:181], v[58:59], v[166:167], v[180:181]
	v_pk_fma_f32 v[178:179], v[56:57], v[166:167], v[178:179]
	v_pk_fma_f32 v[176:177], v[54:55], v[166:167], v[176:177]
	v_pk_fma_f32 v[174:175], v[52:53], v[166:167], v[174:175]
	v_pk_fma_f32 v[172:173], v[50:51], v[166:167], v[172:173]
	v_pk_fma_f32 v[170:171], v[48:49], v[166:167], v[170:171]
	v_pk_fma_f32 v[168:169], v[46:47], v[166:167], v[168:169]
	v_pk_fma_f32 v[166:167], v[106:107], v[166:167], v[108:109]
	v_pk_fma_f32 v[224:225], v[78:79], v[164:165], v[224:225]
	v_pk_fma_f32 v[222:223], v[76:77], v[164:165], v[222:223]
	v_pk_fma_f32 v[220:221], v[74:75], v[164:165], v[220:221]
	v_pk_fma_f32 v[216:217], v[72:73], v[164:165], v[216:217]
	v_pk_fma_f32 v[214:215], v[70:71], v[164:165], v[214:215]
	v_pk_fma_f32 v[212:213], v[68:69], v[164:165], v[212:213]
	v_pk_fma_f32 v[186:187], v[66:67], v[164:165], v[186:187]
	v_pk_fma_f32 v[184:185], v[64:65], v[164:165], v[184:185]
	v_pk_fma_f32 v[182:183], v[62:63], v[164:165], v[182:183]
	v_pk_fma_f32 v[180:181], v[60:61], v[164:165], v[180:181]
	v_pk_fma_f32 v[178:179], v[58:59], v[164:165], v[178:179]
	v_pk_fma_f32 v[176:177], v[56:57], v[164:165], v[176:177]
	v_pk_fma_f32 v[174:175], v[54:55], v[164:165], v[174:175]
	v_pk_fma_f32 v[172:173], v[52:53], v[164:165], v[172:173]
	v_pk_fma_f32 v[170:171], v[50:51], v[164:165], v[170:171]
	v_pk_fma_f32 v[168:169], v[48:49], v[164:165], v[168:169]
	v_pk_fma_f32 v[166:167], v[46:47], v[164:165], v[166:167]
	v_pk_fma_f32 v[164:165], v[106:107], v[164:165], v[108:109]
	v_lshlrev_b32_e32 v20, 16, v21
	v_and_b32_e32 v21, 0xffff0000, v21
	v_pk_fma_f32 v[224:225], v[80:81], v[160:161], v[224:225]
	v_pk_fma_f32 v[222:223], v[78:79], v[160:161], v[222:223]
	v_pk_fma_f32 v[220:221], v[76:77], v[160:161], v[220:221]
	v_pk_fma_f32 v[216:217], v[74:75], v[160:161], v[216:217]
	v_pk_fma_f32 v[214:215], v[72:73], v[160:161], v[214:215]
	v_pk_fma_f32 v[212:213], v[70:71], v[160:161], v[212:213]
	v_pk_fma_f32 v[186:187], v[68:69], v[160:161], v[186:187]
	v_pk_fma_f32 v[184:185], v[66:67], v[160:161], v[184:185]
	v_pk_fma_f32 v[182:183], v[64:65], v[160:161], v[182:183]
	v_pk_fma_f32 v[180:181], v[62:63], v[160:161], v[180:181]
	v_pk_fma_f32 v[178:179], v[60:61], v[160:161], v[178:179]
	v_pk_fma_f32 v[176:177], v[58:59], v[160:161], v[176:177]
	v_pk_fma_f32 v[174:175], v[56:57], v[160:161], v[174:175]
	v_pk_fma_f32 v[172:173], v[54:55], v[160:161], v[172:173]
	v_pk_fma_f32 v[170:171], v[52:53], v[160:161], v[170:171]
	v_pk_fma_f32 v[168:169], v[50:51], v[160:161], v[168:169]
	v_pk_fma_f32 v[166:167], v[48:49], v[160:161], v[166:167]
	v_pk_fma_f32 v[164:165], v[46:47], v[160:161], v[164:165]
	v_pk_fma_f32 v[160:161], v[106:107], v[160:161], v[108:109]
	v_lshlrev_b32_e32 v18, 16, v19
	v_and_b32_e32 v19, 0xffff0000, v19
	v_pk_fma_f32 v[224:225], v[82:83], v[20:21], v[224:225]
	v_pk_fma_f32 v[222:223], v[80:81], v[20:21], v[222:223]
	v_pk_fma_f32 v[220:221], v[78:79], v[20:21], v[220:221]
	v_pk_fma_f32 v[216:217], v[76:77], v[20:21], v[216:217]
	v_pk_fma_f32 v[214:215], v[74:75], v[20:21], v[214:215]
	v_pk_fma_f32 v[212:213], v[72:73], v[20:21], v[212:213]
	v_pk_fma_f32 v[186:187], v[70:71], v[20:21], v[186:187]
	v_pk_fma_f32 v[184:185], v[68:69], v[20:21], v[184:185]
	v_pk_fma_f32 v[182:183], v[66:67], v[20:21], v[182:183]
	v_pk_fma_f32 v[180:181], v[64:65], v[20:21], v[180:181]
	v_pk_fma_f32 v[178:179], v[62:63], v[20:21], v[178:179]
	v_pk_fma_f32 v[176:177], v[60:61], v[20:21], v[176:177]
	v_pk_fma_f32 v[174:175], v[58:59], v[20:21], v[174:175]
	v_pk_fma_f32 v[172:173], v[56:57], v[20:21], v[172:173]
	v_pk_fma_f32 v[170:171], v[54:55], v[20:21], v[170:171]
	v_pk_fma_f32 v[168:169], v[52:53], v[20:21], v[168:169]
	v_pk_fma_f32 v[166:167], v[50:51], v[20:21], v[166:167]
	v_pk_fma_f32 v[164:165], v[48:49], v[20:21], v[164:165]
	v_pk_fma_f32 v[160:161], v[46:47], v[20:21], v[160:161]
	v_pk_fma_f32 v[20:21], v[106:107], v[20:21], v[108:109]
	v_lshlrev_b32_e32 v16, 16, v17
	v_and_b32_e32 v17, 0xffff0000, v17
	v_pk_fma_f32 v[224:225], v[84:85], v[18:19], v[224:225]
	v_pk_fma_f32 v[222:223], v[82:83], v[18:19], v[222:223]
	v_pk_fma_f32 v[220:221], v[80:81], v[18:19], v[220:221]
	v_pk_fma_f32 v[216:217], v[78:79], v[18:19], v[216:217]
	v_pk_fma_f32 v[214:215], v[76:77], v[18:19], v[214:215]
	v_pk_fma_f32 v[212:213], v[74:75], v[18:19], v[212:213]
	v_pk_fma_f32 v[186:187], v[72:73], v[18:19], v[186:187]
	v_pk_fma_f32 v[184:185], v[70:71], v[18:19], v[184:185]
	v_pk_fma_f32 v[182:183], v[68:69], v[18:19], v[182:183]
	v_pk_fma_f32 v[180:181], v[66:67], v[18:19], v[180:181]
	v_pk_fma_f32 v[178:179], v[64:65], v[18:19], v[178:179]
	v_pk_fma_f32 v[176:177], v[62:63], v[18:19], v[176:177]
	v_pk_fma_f32 v[174:175], v[60:61], v[18:19], v[174:175]
	v_pk_fma_f32 v[172:173], v[58:59], v[18:19], v[172:173]
	v_pk_fma_f32 v[170:171], v[56:57], v[18:19], v[170:171]
	v_pk_fma_f32 v[168:169], v[54:55], v[18:19], v[168:169]
	v_pk_fma_f32 v[166:167], v[52:53], v[18:19], v[166:167]
	v_pk_fma_f32 v[164:165], v[50:51], v[18:19], v[164:165]
	v_pk_fma_f32 v[160:161], v[48:49], v[18:19], v[160:161]
	v_pk_fma_f32 v[20:21], v[46:47], v[18:19], v[20:21]
	v_pk_fma_f32 v[18:19], v[106:107], v[18:19], v[108:109]
	v_lshlrev_b32_e32 v14, 16, v15
	v_and_b32_e32 v15, 0xffff0000, v15
	v_pk_fma_f32 v[224:225], v[86:87], v[16:17], v[224:225]
	v_pk_fma_f32 v[222:223], v[84:85], v[16:17], v[222:223]
	v_pk_fma_f32 v[220:221], v[82:83], v[16:17], v[220:221]
	v_pk_fma_f32 v[216:217], v[80:81], v[16:17], v[216:217]
	v_pk_fma_f32 v[214:215], v[78:79], v[16:17], v[214:215]
	v_pk_fma_f32 v[212:213], v[76:77], v[16:17], v[212:213]
	v_pk_fma_f32 v[186:187], v[74:75], v[16:17], v[186:187]
	v_pk_fma_f32 v[184:185], v[72:73], v[16:17], v[184:185]
	v_pk_fma_f32 v[182:183], v[70:71], v[16:17], v[182:183]
	v_pk_fma_f32 v[180:181], v[68:69], v[16:17], v[180:181]
	v_pk_fma_f32 v[178:179], v[66:67], v[16:17], v[178:179]
	v_pk_fma_f32 v[176:177], v[64:65], v[16:17], v[176:177]
	v_pk_fma_f32 v[174:175], v[62:63], v[16:17], v[174:175]
	v_pk_fma_f32 v[172:173], v[60:61], v[16:17], v[172:173]
	v_pk_fma_f32 v[170:171], v[58:59], v[16:17], v[170:171]
	v_pk_fma_f32 v[168:169], v[56:57], v[16:17], v[168:169]
	v_pk_fma_f32 v[166:167], v[54:55], v[16:17], v[166:167]
	v_pk_fma_f32 v[164:165], v[52:53], v[16:17], v[164:165]
	v_pk_fma_f32 v[160:161], v[50:51], v[16:17], v[160:161]
	v_pk_fma_f32 v[20:21], v[48:49], v[16:17], v[20:21]
	v_pk_fma_f32 v[18:19], v[46:47], v[16:17], v[18:19]
	v_pk_fma_f32 v[16:17], v[106:107], v[16:17], v[108:109]
	v_lshlrev_b32_e32 v12, 16, v13
	v_and_b32_e32 v13, 0xffff0000, v13
	v_pk_fma_f32 v[224:225], v[88:89], v[14:15], v[224:225]
	v_pk_fma_f32 v[222:223], v[86:87], v[14:15], v[222:223]
	v_pk_fma_f32 v[220:221], v[84:85], v[14:15], v[220:221]
	v_pk_fma_f32 v[216:217], v[82:83], v[14:15], v[216:217]
	v_pk_fma_f32 v[214:215], v[80:81], v[14:15], v[214:215]
	v_pk_fma_f32 v[212:213], v[78:79], v[14:15], v[212:213]
	v_pk_fma_f32 v[186:187], v[76:77], v[14:15], v[186:187]
	v_pk_fma_f32 v[184:185], v[74:75], v[14:15], v[184:185]
	v_pk_fma_f32 v[182:183], v[72:73], v[14:15], v[182:183]
	v_pk_fma_f32 v[180:181], v[70:71], v[14:15], v[180:181]
	v_pk_fma_f32 v[178:179], v[68:69], v[14:15], v[178:179]
	v_pk_fma_f32 v[176:177], v[66:67], v[14:15], v[176:177]
	v_pk_fma_f32 v[174:175], v[64:65], v[14:15], v[174:175]
	v_pk_fma_f32 v[172:173], v[62:63], v[14:15], v[172:173]
	v_pk_fma_f32 v[170:171], v[60:61], v[14:15], v[170:171]
	v_pk_fma_f32 v[168:169], v[58:59], v[14:15], v[168:169]
	v_pk_fma_f32 v[166:167], v[56:57], v[14:15], v[166:167]
	v_pk_fma_f32 v[164:165], v[54:55], v[14:15], v[164:165]
	v_pk_fma_f32 v[160:161], v[52:53], v[14:15], v[160:161]
	v_pk_fma_f32 v[20:21], v[50:51], v[14:15], v[20:21]
	v_pk_fma_f32 v[18:19], v[48:49], v[14:15], v[18:19]
	v_pk_fma_f32 v[16:17], v[46:47], v[14:15], v[16:17]
	v_pk_fma_f32 v[14:15], v[106:107], v[14:15], v[108:109]
	v_lshlrev_b32_e32 v10, 16, v11
	v_and_b32_e32 v11, 0xffff0000, v11
	v_pk_fma_f32 v[224:225], v[90:91], v[12:13], v[224:225]
	v_pk_fma_f32 v[222:223], v[88:89], v[12:13], v[222:223]
	v_pk_fma_f32 v[220:221], v[86:87], v[12:13], v[220:221]
	v_pk_fma_f32 v[216:217], v[84:85], v[12:13], v[216:217]
	v_pk_fma_f32 v[214:215], v[82:83], v[12:13], v[214:215]
	v_pk_fma_f32 v[212:213], v[80:81], v[12:13], v[212:213]
	v_pk_fma_f32 v[186:187], v[78:79], v[12:13], v[186:187]
	v_pk_fma_f32 v[184:185], v[76:77], v[12:13], v[184:185]
	v_pk_fma_f32 v[182:183], v[74:75], v[12:13], v[182:183]
	v_pk_fma_f32 v[180:181], v[72:73], v[12:13], v[180:181]
	v_pk_fma_f32 v[178:179], v[70:71], v[12:13], v[178:179]
	v_pk_fma_f32 v[176:177], v[68:69], v[12:13], v[176:177]
	v_pk_fma_f32 v[174:175], v[66:67], v[12:13], v[174:175]
	v_pk_fma_f32 v[172:173], v[64:65], v[12:13], v[172:173]
	v_pk_fma_f32 v[170:171], v[62:63], v[12:13], v[170:171]
	v_pk_fma_f32 v[168:169], v[60:61], v[12:13], v[168:169]
	v_pk_fma_f32 v[166:167], v[58:59], v[12:13], v[166:167]
	v_pk_fma_f32 v[164:165], v[56:57], v[12:13], v[164:165]
	v_pk_fma_f32 v[160:161], v[54:55], v[12:13], v[160:161]
	v_pk_fma_f32 v[20:21], v[52:53], v[12:13], v[20:21]
	v_pk_fma_f32 v[18:19], v[50:51], v[12:13], v[18:19]
	v_pk_fma_f32 v[16:17], v[48:49], v[12:13], v[16:17]
	v_pk_fma_f32 v[14:15], v[46:47], v[12:13], v[14:15]
	v_pk_fma_f32 v[12:13], v[106:107], v[12:13], v[108:109]
	v_lshlrev_b32_e32 v8, 16, v9
	v_and_b32_e32 v9, 0xffff0000, v9
	v_pk_fma_f32 v[224:225], v[92:93], v[10:11], v[224:225]
	v_pk_fma_f32 v[222:223], v[90:91], v[10:11], v[222:223]
	v_pk_fma_f32 v[220:221], v[88:89], v[10:11], v[220:221]
	v_pk_fma_f32 v[216:217], v[86:87], v[10:11], v[216:217]
	v_pk_fma_f32 v[214:215], v[84:85], v[10:11], v[214:215]
	v_pk_fma_f32 v[212:213], v[82:83], v[10:11], v[212:213]
	v_pk_fma_f32 v[186:187], v[80:81], v[10:11], v[186:187]
	v_pk_fma_f32 v[184:185], v[78:79], v[10:11], v[184:185]
	v_pk_fma_f32 v[182:183], v[76:77], v[10:11], v[182:183]
	v_pk_fma_f32 v[180:181], v[74:75], v[10:11], v[180:181]
	v_pk_fma_f32 v[178:179], v[72:73], v[10:11], v[178:179]
	v_pk_fma_f32 v[176:177], v[70:71], v[10:11], v[176:177]
	v_pk_fma_f32 v[174:175], v[68:69], v[10:11], v[174:175]
	v_pk_fma_f32 v[172:173], v[66:67], v[10:11], v[172:173]
	v_pk_fma_f32 v[170:171], v[64:65], v[10:11], v[170:171]
	v_pk_fma_f32 v[168:169], v[62:63], v[10:11], v[168:169]
	v_pk_fma_f32 v[166:167], v[60:61], v[10:11], v[166:167]
	v_pk_fma_f32 v[164:165], v[58:59], v[10:11], v[164:165]
	v_pk_fma_f32 v[160:161], v[56:57], v[10:11], v[160:161]
	v_pk_fma_f32 v[20:21], v[54:55], v[10:11], v[20:21]
	v_pk_fma_f32 v[18:19], v[52:53], v[10:11], v[18:19]
	v_pk_fma_f32 v[16:17], v[50:51], v[10:11], v[16:17]
	v_pk_fma_f32 v[14:15], v[48:49], v[10:11], v[14:15]
	v_pk_fma_f32 v[12:13], v[46:47], v[10:11], v[12:13]
	v_pk_fma_f32 v[10:11], v[106:107], v[10:11], v[108:109]
	v_lshlrev_b32_e32 v6, 16, v7
	v_and_b32_e32 v7, 0xffff0000, v7
	v_pk_fma_f32 v[224:225], v[94:95], v[8:9], v[224:225]
	v_pk_fma_f32 v[222:223], v[92:93], v[8:9], v[222:223]
	v_pk_fma_f32 v[220:221], v[90:91], v[8:9], v[220:221]
	v_pk_fma_f32 v[216:217], v[88:89], v[8:9], v[216:217]
	v_pk_fma_f32 v[214:215], v[86:87], v[8:9], v[214:215]
	v_pk_fma_f32 v[212:213], v[84:85], v[8:9], v[212:213]
	v_pk_fma_f32 v[186:187], v[82:83], v[8:9], v[186:187]
	v_pk_fma_f32 v[184:185], v[80:81], v[8:9], v[184:185]
	v_pk_fma_f32 v[182:183], v[78:79], v[8:9], v[182:183]
	v_pk_fma_f32 v[180:181], v[76:77], v[8:9], v[180:181]
	v_pk_fma_f32 v[178:179], v[74:75], v[8:9], v[178:179]
	v_pk_fma_f32 v[176:177], v[72:73], v[8:9], v[176:177]
	v_pk_fma_f32 v[174:175], v[70:71], v[8:9], v[174:175]
	v_pk_fma_f32 v[172:173], v[68:69], v[8:9], v[172:173]
	v_pk_fma_f32 v[170:171], v[66:67], v[8:9], v[170:171]
	v_pk_fma_f32 v[168:169], v[64:65], v[8:9], v[168:169]
	v_pk_fma_f32 v[166:167], v[62:63], v[8:9], v[166:167]
	v_pk_fma_f32 v[164:165], v[60:61], v[8:9], v[164:165]
	v_pk_fma_f32 v[160:161], v[58:59], v[8:9], v[160:161]
	v_pk_fma_f32 v[20:21], v[56:57], v[8:9], v[20:21]
	v_pk_fma_f32 v[18:19], v[54:55], v[8:9], v[18:19]
	v_pk_fma_f32 v[16:17], v[52:53], v[8:9], v[16:17]
	v_pk_fma_f32 v[14:15], v[50:51], v[8:9], v[14:15]
	v_pk_fma_f32 v[12:13], v[48:49], v[8:9], v[12:13]
	v_pk_fma_f32 v[10:11], v[46:47], v[8:9], v[10:11]
	v_pk_fma_f32 v[8:9], v[106:107], v[8:9], v[108:109]
	v_lshlrev_b32_e32 v4, 16, v5
	v_and_b32_e32 v5, 0xffff0000, v5
	v_pk_fma_f32 v[224:225], v[96:97], v[6:7], v[224:225]
	v_pk_fma_f32 v[222:223], v[94:95], v[6:7], v[222:223]
	v_pk_fma_f32 v[220:221], v[92:93], v[6:7], v[220:221]
	v_pk_fma_f32 v[216:217], v[90:91], v[6:7], v[216:217]
	v_pk_fma_f32 v[214:215], v[88:89], v[6:7], v[214:215]
	v_pk_fma_f32 v[212:213], v[86:87], v[6:7], v[212:213]
	v_pk_fma_f32 v[186:187], v[84:85], v[6:7], v[186:187]
	v_pk_fma_f32 v[184:185], v[82:83], v[6:7], v[184:185]
	v_pk_fma_f32 v[182:183], v[80:81], v[6:7], v[182:183]
	v_pk_fma_f32 v[180:181], v[78:79], v[6:7], v[180:181]
	v_pk_fma_f32 v[178:179], v[76:77], v[6:7], v[178:179]
	v_pk_fma_f32 v[176:177], v[74:75], v[6:7], v[176:177]
	v_pk_fma_f32 v[174:175], v[72:73], v[6:7], v[174:175]
	v_pk_fma_f32 v[172:173], v[70:71], v[6:7], v[172:173]
	v_pk_fma_f32 v[170:171], v[68:69], v[6:7], v[170:171]
	v_pk_fma_f32 v[168:169], v[66:67], v[6:7], v[168:169]
	v_pk_fma_f32 v[166:167], v[64:65], v[6:7], v[166:167]
	v_pk_fma_f32 v[164:165], v[62:63], v[6:7], v[164:165]
	v_pk_fma_f32 v[160:161], v[60:61], v[6:7], v[160:161]
	v_pk_fma_f32 v[20:21], v[58:59], v[6:7], v[20:21]
	v_pk_fma_f32 v[18:19], v[56:57], v[6:7], v[18:19]
	v_pk_fma_f32 v[16:17], v[54:55], v[6:7], v[16:17]
	v_pk_fma_f32 v[14:15], v[52:53], v[6:7], v[14:15]
	v_pk_fma_f32 v[12:13], v[50:51], v[6:7], v[12:13]
	v_pk_fma_f32 v[10:11], v[48:49], v[6:7], v[10:11]
	v_pk_fma_f32 v[8:9], v[46:47], v[6:7], v[8:9]
	v_pk_fma_f32 v[6:7], v[106:107], v[6:7], v[108:109]
	v_lshlrev_b32_e32 v2, 16, v3
	v_and_b32_e32 v3, 0xffff0000, v3
	v_pk_fma_f32 v[224:225], v[98:99], v[4:5], v[224:225]
	v_pk_fma_f32 v[222:223], v[96:97], v[4:5], v[222:223]
	v_pk_fma_f32 v[220:221], v[94:95], v[4:5], v[220:221]
	v_pk_fma_f32 v[216:217], v[92:93], v[4:5], v[216:217]
	v_pk_fma_f32 v[214:215], v[90:91], v[4:5], v[214:215]
	v_pk_fma_f32 v[212:213], v[88:89], v[4:5], v[212:213]
	v_pk_fma_f32 v[186:187], v[86:87], v[4:5], v[186:187]
	v_pk_fma_f32 v[184:185], v[84:85], v[4:5], v[184:185]
	v_pk_fma_f32 v[182:183], v[82:83], v[4:5], v[182:183]
	v_pk_fma_f32 v[180:181], v[80:81], v[4:5], v[180:181]
	v_pk_fma_f32 v[178:179], v[78:79], v[4:5], v[178:179]
	v_pk_fma_f32 v[176:177], v[76:77], v[4:5], v[176:177]
	v_pk_fma_f32 v[174:175], v[74:75], v[4:5], v[174:175]
	v_pk_fma_f32 v[172:173], v[72:73], v[4:5], v[172:173]
	v_pk_fma_f32 v[170:171], v[70:71], v[4:5], v[170:171]
	v_pk_fma_f32 v[168:169], v[68:69], v[4:5], v[168:169]
	v_pk_fma_f32 v[166:167], v[66:67], v[4:5], v[166:167]
	v_pk_fma_f32 v[164:165], v[64:65], v[4:5], v[164:165]
	v_pk_fma_f32 v[160:161], v[62:63], v[4:5], v[160:161]
	v_pk_fma_f32 v[20:21], v[60:61], v[4:5], v[20:21]
	v_pk_fma_f32 v[18:19], v[58:59], v[4:5], v[18:19]
	v_pk_fma_f32 v[16:17], v[56:57], v[4:5], v[16:17]
	v_pk_fma_f32 v[14:15], v[54:55], v[4:5], v[14:15]
	v_pk_fma_f32 v[12:13], v[52:53], v[4:5], v[12:13]
	v_pk_fma_f32 v[10:11], v[50:51], v[4:5], v[10:11]
	v_pk_fma_f32 v[8:9], v[48:49], v[4:5], v[8:9]
	v_pk_fma_f32 v[6:7], v[46:47], v[4:5], v[6:7]
	v_pk_fma_f32 v[4:5], v[106:107], v[4:5], v[108:109]
	v_lshlrev_b32_e32 v162, 16, v30
	v_and_b32_e32 v163, 0xffff0000, v30
	v_pk_fma_f32 v[224:225], v[100:101], v[2:3], v[224:225]
	v_pk_fma_f32 v[222:223], v[98:99], v[2:3], v[222:223]
	v_pk_fma_f32 v[220:221], v[96:97], v[2:3], v[220:221]
	v_pk_fma_f32 v[216:217], v[94:95], v[2:3], v[216:217]
	v_pk_fma_f32 v[214:215], v[92:93], v[2:3], v[214:215]
	v_pk_fma_f32 v[212:213], v[90:91], v[2:3], v[212:213]
	v_pk_fma_f32 v[186:187], v[88:89], v[2:3], v[186:187]
	v_pk_fma_f32 v[184:185], v[86:87], v[2:3], v[184:185]
	v_pk_fma_f32 v[182:183], v[84:85], v[2:3], v[182:183]
	v_pk_fma_f32 v[180:181], v[82:83], v[2:3], v[180:181]
	v_pk_fma_f32 v[178:179], v[80:81], v[2:3], v[178:179]
	v_pk_fma_f32 v[176:177], v[78:79], v[2:3], v[176:177]
	v_pk_fma_f32 v[174:175], v[76:77], v[2:3], v[174:175]
	v_pk_fma_f32 v[172:173], v[74:75], v[2:3], v[172:173]
	v_pk_fma_f32 v[170:171], v[72:73], v[2:3], v[170:171]
	v_pk_fma_f32 v[168:169], v[70:71], v[2:3], v[168:169]
	v_pk_fma_f32 v[166:167], v[68:69], v[2:3], v[166:167]
	v_pk_fma_f32 v[164:165], v[66:67], v[2:3], v[164:165]
	v_pk_fma_f32 v[160:161], v[64:65], v[2:3], v[160:161]
	v_pk_fma_f32 v[20:21], v[62:63], v[2:3], v[20:21]
	v_pk_fma_f32 v[18:19], v[60:61], v[2:3], v[18:19]
	v_pk_fma_f32 v[16:17], v[58:59], v[2:3], v[16:17]
	v_pk_fma_f32 v[14:15], v[56:57], v[2:3], v[14:15]
	v_pk_fma_f32 v[12:13], v[54:55], v[2:3], v[12:13]
	v_pk_fma_f32 v[10:11], v[52:53], v[2:3], v[10:11]
	v_pk_fma_f32 v[8:9], v[50:51], v[2:3], v[8:9]
	v_pk_fma_f32 v[6:7], v[48:49], v[2:3], v[6:7]
	v_pk_fma_f32 v[4:5], v[46:47], v[2:3], v[4:5]
	v_pk_fma_f32 v[2:3], v[106:107], v[2:3], v[108:109]
	s_waitcnt vmcnt(30)
	v_lshlrev_b32_e32 v158, 16, v31
	v_and_b32_e32 v159, 0xffff0000, v31
	v_pk_fma_f32 v[2:3], v[46:47], v[162:163], v[2:3]
	s_waitcnt vmcnt(29)
	v_lshlrev_b32_e32 v22, 16, v122
	v_and_b32_e32 v23, 0xffff0000, v122
	v_pk_fma_f32 v[2:3], v[48:49], v[158:159], v[2:3]
	s_waitcnt vmcnt(28)
	v_lshlrev_b32_e32 v24, 16, v123
	v_and_b32_e32 v25, 0xffff0000, v123
	v_pk_fma_f32 v[2:3], v[50:51], v[22:23], v[2:3]
	s_ashr_i32 s5, s4, 31
	s_waitcnt vmcnt(27)
	v_lshlrev_b32_e32 v26, 16, v124
	v_and_b32_e32 v27, 0xffff0000, v124
	v_pk_fma_f32 v[2:3], v[52:53], v[24:25], v[2:3]
	s_lshl_b64 s[0:1], s[4:5], 11
	s_waitcnt vmcnt(26)
	v_lshlrev_b32_e32 v28, 16, v125
	v_and_b32_e32 v29, 0xffff0000, v125
	v_pk_fma_f32 v[2:3], v[54:55], v[26:27], v[2:3]
	v_lshl_add_u64 v[32:33], v[110:111], 0, s[0:1]
	s_waitcnt vmcnt(25)
	v_lshlrev_b32_e32 v30, 16, v126
	v_and_b32_e32 v31, 0xffff0000, v126
	v_pk_fma_f32 v[2:3], v[56:57], v[28:29], v[2:3]
	global_load_dword v157, v[32:33], off
	s_waitcnt vmcnt(25)
	v_lshlrev_b32_e32 v32, 16, v127
	v_and_b32_e32 v33, 0xffff0000, v127
	v_pk_fma_f32 v[2:3], v[58:59], v[30:31], v[2:3]
	s_waitcnt vmcnt(24)
	v_lshlrev_b32_e32 v34, 16, v128
	v_and_b32_e32 v35, 0xffff0000, v128
	v_pk_fma_f32 v[2:3], v[60:61], v[32:33], v[2:3]
	s_waitcnt vmcnt(23)
	v_lshlrev_b32_e32 v36, 16, v129
	v_and_b32_e32 v37, 0xffff0000, v129
	v_pk_fma_f32 v[2:3], v[62:63], v[34:35], v[2:3]
	s_waitcnt vmcnt(22)
	v_lshlrev_b32_e32 v38, 16, v130
	v_and_b32_e32 v39, 0xffff0000, v130
	v_pk_fma_f32 v[2:3], v[64:65], v[36:37], v[2:3]
	s_waitcnt vmcnt(21)
	v_lshlrev_b32_e32 v40, 16, v131
	v_and_b32_e32 v41, 0xffff0000, v131
	v_pk_fma_f32 v[2:3], v[66:67], v[38:39], v[2:3]
	s_waitcnt vmcnt(20)
	v_lshlrev_b32_e32 v42, 16, v132
	v_and_b32_e32 v43, 0xffff0000, v132
	v_pk_fma_f32 v[2:3], v[68:69], v[40:41], v[2:3]
	s_waitcnt vmcnt(19)
	v_lshlrev_b32_e32 v44, 16, v133
	v_and_b32_e32 v45, 0xffff0000, v133
	v_pk_fma_f32 v[2:3], v[70:71], v[42:43], v[2:3]
	s_waitcnt vmcnt(18)
	v_lshlrev_b32_e32 v120, 16, v134
	v_and_b32_e32 v121, 0xffff0000, v134
	v_pk_fma_f32 v[2:3], v[72:73], v[44:45], v[2:3]
	s_waitcnt vmcnt(17)
	v_lshlrev_b32_e32 v122, 16, v135
	v_and_b32_e32 v123, 0xffff0000, v135
	v_pk_fma_f32 v[2:3], v[74:75], v[120:121], v[2:3]
	s_waitcnt vmcnt(16)
	v_lshlrev_b32_e32 v124, 16, v136
	v_and_b32_e32 v125, 0xffff0000, v136
	v_pk_fma_f32 v[2:3], v[76:77], v[122:123], v[2:3]
	s_waitcnt vmcnt(15)
	v_lshlrev_b32_e32 v126, 16, v137
	v_and_b32_e32 v127, 0xffff0000, v137
	v_pk_fma_f32 v[2:3], v[78:79], v[124:125], v[2:3]
	s_waitcnt vmcnt(14)
	v_lshlrev_b32_e32 v128, 16, v138
	v_and_b32_e32 v129, 0xffff0000, v138
	v_pk_fma_f32 v[2:3], v[80:81], v[126:127], v[2:3]
	s_waitcnt vmcnt(13)
	v_lshlrev_b32_e32 v130, 16, v139
	v_and_b32_e32 v131, 0xffff0000, v139
	v_pk_fma_f32 v[2:3], v[82:83], v[128:129], v[2:3]
	s_waitcnt vmcnt(12)
	v_lshlrev_b32_e32 v134, 16, v140
	v_and_b32_e32 v135, 0xffff0000, v140
	v_pk_fma_f32 v[2:3], v[84:85], v[130:131], v[2:3]
	s_waitcnt vmcnt(11)
	v_lshlrev_b32_e32 v138, 16, v141
	v_and_b32_e32 v139, 0xffff0000, v141
	v_pk_fma_f32 v[2:3], v[86:87], v[134:135], v[2:3]
	s_waitcnt vmcnt(10)
	v_lshlrev_b32_e32 v132, 16, v142
	v_and_b32_e32 v133, 0xffff0000, v142
	v_pk_fma_f32 v[2:3], v[88:89], v[138:139], v[2:3]
	s_waitcnt vmcnt(9)
	v_lshlrev_b32_e32 v136, 16, v143
	v_and_b32_e32 v137, 0xffff0000, v143
	v_pk_fma_f32 v[2:3], v[90:91], v[132:133], v[2:3]
	s_waitcnt vmcnt(8)
	v_lshlrev_b32_e32 v140, 16, v144
	v_and_b32_e32 v141, 0xffff0000, v144
	v_pk_fma_f32 v[2:3], v[92:93], v[136:137], v[2:3]
	s_waitcnt vmcnt(7)
	v_lshlrev_b32_e32 v142, 16, v145
	v_and_b32_e32 v143, 0xffff0000, v145
	v_pk_fma_f32 v[2:3], v[94:95], v[140:141], v[2:3]
	s_waitcnt vmcnt(6)
	v_lshlrev_b32_e32 v144, 16, v146
	v_and_b32_e32 v145, 0xffff0000, v146
	v_pk_fma_f32 v[2:3], v[96:97], v[142:143], v[2:3]
	s_waitcnt vmcnt(5)
	v_lshlrev_b32_e32 v146, 16, v147
	v_and_b32_e32 v147, 0xffff0000, v147
	v_pk_fma_f32 v[2:3], v[98:99], v[144:145], v[2:3]
	s_waitcnt vmcnt(4)
	v_lshlrev_b32_e32 v148, 16, v149
	v_and_b32_e32 v149, 0xffff0000, v149
	v_pk_fma_f32 v[2:3], v[100:101], v[146:147], v[2:3]
	s_waitcnt vmcnt(3)
	v_lshlrev_b32_e32 v150, 16, v151
	v_and_b32_e32 v151, 0xffff0000, v151
	v_pk_fma_f32 v[2:3], v[102:103], v[148:149], v[2:3]
	s_nop 0
	v_pk_fma_f32 v[2:3], v[104:105], v[150:151], v[2:3]
	s_barrier
	ds_write_b64 v201, v[2:3]
	v_pk_fma_f32 v[2:3], v[106:107], v[162:163], v[108:109]
	s_waitcnt vmcnt(2)
	v_lshlrev_b32_e32 v152, 16, v153
	v_pk_fma_f32 v[2:3], v[46:47], v[158:159], v[2:3]
	v_and_b32_e32 v153, 0xffff0000, v153
	v_pk_fma_f32 v[2:3], v[48:49], v[22:23], v[2:3]
	s_waitcnt vmcnt(1)
	v_lshlrev_b32_e32 v154, 16, v155
	v_pk_fma_f32 v[2:3], v[50:51], v[24:25], v[2:3]
	v_and_b32_e32 v155, 0xffff0000, v155
	v_pk_fma_f32 v[2:3], v[52:53], v[26:27], v[2:3]
	v_pk_fma_f32 v[4:5], v[48:49], v[162:163], v[4:5]
	v_pk_fma_f32 v[2:3], v[54:55], v[28:29], v[2:3]
	v_pk_fma_f32 v[8:9], v[52:53], v[162:163], v[8:9]
	v_pk_fma_f32 v[2:3], v[56:57], v[30:31], v[2:3]
	v_pk_fma_f32 v[6:7], v[50:51], v[162:163], v[6:7]
	v_pk_fma_f32 v[2:3], v[58:59], v[32:33], v[2:3]
	v_pk_fma_f32 v[4:5], v[50:51], v[158:159], v[4:5]
	v_pk_fma_f32 v[2:3], v[60:61], v[34:35], v[2:3]
	v_pk_fma_f32 v[8:9], v[54:55], v[158:159], v[8:9]
	v_pk_fma_f32 v[2:3], v[62:63], v[36:37], v[2:3]
	v_pk_fma_f32 v[6:7], v[52:53], v[158:159], v[6:7]
	v_pk_fma_f32 v[2:3], v[64:65], v[38:39], v[2:3]
	v_pk_fma_f32 v[4:5], v[52:53], v[22:23], v[4:5]
	v_pk_fma_f32 v[2:3], v[66:67], v[40:41], v[2:3]
	v_pk_fma_f32 v[10:11], v[54:55], v[162:163], v[10:11]
	v_pk_fma_f32 v[2:3], v[68:69], v[42:43], v[2:3]
	v_pk_fma_f32 v[8:9], v[56:57], v[22:23], v[8:9]
	v_pk_fma_f32 v[2:3], v[70:71], v[44:45], v[2:3]
	v_pk_fma_f32 v[6:7], v[54:55], v[22:23], v[6:7]
	v_pk_fma_f32 v[2:3], v[72:73], v[120:121], v[2:3]
	v_pk_fma_f32 v[4:5], v[54:55], v[24:25], v[4:5]
	v_pk_fma_f32 v[2:3], v[74:75], v[122:123], v[2:3]
	v_pk_fma_f32 v[12:13], v[56:57], v[162:163], v[12:13]
	v_pk_fma_f32 v[2:3], v[76:77], v[124:125], v[2:3]
	v_pk_fma_f32 v[10:11], v[56:57], v[158:159], v[10:11]
	v_pk_fma_f32 v[2:3], v[78:79], v[126:127], v[2:3]
	v_pk_fma_f32 v[8:9], v[58:59], v[24:25], v[8:9]
	v_pk_fma_f32 v[2:3], v[80:81], v[128:129], v[2:3]
	v_pk_fma_f32 v[6:7], v[56:57], v[24:25], v[6:7]
	v_pk_fma_f32 v[2:3], v[82:83], v[130:131], v[2:3]
	v_pk_fma_f32 v[4:5], v[56:57], v[26:27], v[4:5]
	v_pk_fma_f32 v[2:3], v[84:85], v[134:135], v[2:3]
	v_pk_fma_f32 v[14:15], v[58:59], v[162:163], v[14:15]
	v_pk_fma_f32 v[2:3], v[86:87], v[138:139], v[2:3]
	v_pk_fma_f32 v[12:13], v[58:59], v[158:159], v[12:13]
	v_pk_fma_f32 v[2:3], v[88:89], v[132:133], v[2:3]
	v_pk_fma_f32 v[10:11], v[58:59], v[22:23], v[10:11]
	v_pk_fma_f32 v[2:3], v[90:91], v[136:137], v[2:3]
	v_pk_fma_f32 v[8:9], v[60:61], v[26:27], v[8:9]
	v_pk_fma_f32 v[2:3], v[92:93], v[140:141], v[2:3]
	v_pk_fma_f32 v[6:7], v[58:59], v[26:27], v[6:7]
	v_pk_fma_f32 v[2:3], v[94:95], v[142:143], v[2:3]
	v_pk_fma_f32 v[4:5], v[58:59], v[28:29], v[4:5]
	v_pk_fma_f32 v[2:3], v[96:97], v[144:145], v[2:3]
	v_pk_fma_f32 v[16:17], v[60:61], v[162:163], v[16:17]
	v_pk_fma_f32 v[2:3], v[98:99], v[146:147], v[2:3]
	v_pk_fma_f32 v[14:15], v[60:61], v[158:159], v[14:15]
	v_pk_fma_f32 v[2:3], v[100:101], v[148:149], v[2:3]
	v_pk_fma_f32 v[12:13], v[60:61], v[22:23], v[12:13]
	v_pk_fma_f32 v[2:3], v[102:103], v[150:151], v[2:3]
	v_pk_fma_f32 v[10:11], v[60:61], v[24:25], v[10:11]
	v_pk_fma_f32 v[2:3], v[104:105], v[152:153], v[2:3]
	ds_write_b64 v202, v[2:3]
	v_pk_fma_f32 v[2:3], v[106:107], v[158:159], v[108:109]
	v_pk_fma_f32 v[8:9], v[62:63], v[28:29], v[8:9]
	v_pk_fma_f32 v[2:3], v[46:47], v[22:23], v[2:3]
	v_pk_fma_f32 v[6:7], v[60:61], v[28:29], v[6:7]
	v_pk_fma_f32 v[2:3], v[48:49], v[24:25], v[2:3]
	v_pk_fma_f32 v[4:5], v[60:61], v[30:31], v[4:5]
	v_pk_fma_f32 v[2:3], v[50:51], v[26:27], v[2:3]
	v_pk_fma_f32 v[18:19], v[62:63], v[162:163], v[18:19]
	v_pk_fma_f32 v[2:3], v[52:53], v[28:29], v[2:3]
	v_pk_fma_f32 v[16:17], v[62:63], v[158:159], v[16:17]
	v_pk_fma_f32 v[2:3], v[54:55], v[30:31], v[2:3]
	v_pk_fma_f32 v[14:15], v[62:63], v[22:23], v[14:15]
	v_pk_fma_f32 v[2:3], v[56:57], v[32:33], v[2:3]
	v_pk_fma_f32 v[12:13], v[62:63], v[24:25], v[12:13]
	v_pk_fma_f32 v[2:3], v[58:59], v[34:35], v[2:3]
	v_pk_fma_f32 v[10:11], v[62:63], v[26:27], v[10:11]
	v_pk_fma_f32 v[2:3], v[60:61], v[36:37], v[2:3]
	v_pk_fma_f32 v[8:9], v[64:65], v[30:31], v[8:9]
	v_pk_fma_f32 v[2:3], v[62:63], v[38:39], v[2:3]
	v_pk_fma_f32 v[6:7], v[62:63], v[30:31], v[6:7]
	v_pk_fma_f32 v[2:3], v[64:65], v[40:41], v[2:3]
	v_pk_fma_f32 v[4:5], v[62:63], v[32:33], v[4:5]
	v_pk_fma_f32 v[2:3], v[66:67], v[42:43], v[2:3]
	v_pk_fma_f32 v[20:21], v[64:65], v[162:163], v[20:21]
	v_pk_fma_f32 v[2:3], v[68:69], v[44:45], v[2:3]
	v_pk_fma_f32 v[18:19], v[64:65], v[158:159], v[18:19]
	v_pk_fma_f32 v[2:3], v[70:71], v[120:121], v[2:3]
	v_pk_fma_f32 v[16:17], v[64:65], v[22:23], v[16:17]
	v_pk_fma_f32 v[2:3], v[72:73], v[122:123], v[2:3]
	v_pk_fma_f32 v[14:15], v[64:65], v[24:25], v[14:15]
	v_pk_fma_f32 v[2:3], v[74:75], v[124:125], v[2:3]
	v_pk_fma_f32 v[12:13], v[64:65], v[26:27], v[12:13]
	v_pk_fma_f32 v[2:3], v[76:77], v[126:127], v[2:3]
	v_pk_fma_f32 v[10:11], v[64:65], v[28:29], v[10:11]
	v_pk_fma_f32 v[2:3], v[78:79], v[128:129], v[2:3]
	v_pk_fma_f32 v[8:9], v[66:67], v[32:33], v[8:9]
	v_pk_fma_f32 v[2:3], v[80:81], v[130:131], v[2:3]
	v_pk_fma_f32 v[6:7], v[64:65], v[32:33], v[6:7]
	v_pk_fma_f32 v[2:3], v[82:83], v[134:135], v[2:3]
	v_pk_fma_f32 v[4:5], v[64:65], v[34:35], v[4:5]
	v_pk_fma_f32 v[2:3], v[84:85], v[138:139], v[2:3]
	v_pk_fma_f32 v[160:161], v[66:67], v[162:163], v[160:161]
	v_pk_fma_f32 v[2:3], v[86:87], v[132:133], v[2:3]
	v_pk_fma_f32 v[20:21], v[66:67], v[158:159], v[20:21]
	v_pk_fma_f32 v[2:3], v[88:89], v[136:137], v[2:3]
	v_pk_fma_f32 v[18:19], v[66:67], v[22:23], v[18:19]
	v_pk_fma_f32 v[2:3], v[90:91], v[140:141], v[2:3]
	v_pk_fma_f32 v[16:17], v[66:67], v[24:25], v[16:17]
	v_pk_fma_f32 v[2:3], v[92:93], v[142:143], v[2:3]
	v_pk_fma_f32 v[14:15], v[66:67], v[26:27], v[14:15]
	v_pk_fma_f32 v[2:3], v[94:95], v[144:145], v[2:3]
	v_pk_fma_f32 v[12:13], v[66:67], v[28:29], v[12:13]
	v_pk_fma_f32 v[2:3], v[96:97], v[146:147], v[2:3]
	v_pk_fma_f32 v[10:11], v[66:67], v[30:31], v[10:11]
	v_pk_fma_f32 v[2:3], v[98:99], v[148:149], v[2:3]
	v_pk_fma_f32 v[8:9], v[68:69], v[34:35], v[8:9]
	v_pk_fma_f32 v[2:3], v[100:101], v[150:151], v[2:3]
	v_pk_fma_f32 v[6:7], v[66:67], v[34:35], v[6:7]
	v_pk_fma_f32 v[2:3], v[102:103], v[152:153], v[2:3]
	v_pk_fma_f32 v[4:5], v[66:67], v[36:37], v[4:5]
	v_pk_fma_f32 v[2:3], v[104:105], v[154:155], v[2:3]
	ds_write_b64 v203, v[2:3]
	v_pk_fma_f32 v[2:3], v[106:107], v[22:23], v[108:109]
	v_pk_fma_f32 v[164:165], v[68:69], v[162:163], v[164:165]
	v_pk_fma_f32 v[2:3], v[46:47], v[24:25], v[2:3]
	v_pk_fma_f32 v[160:161], v[68:69], v[158:159], v[160:161]
	v_pk_fma_f32 v[2:3], v[48:49], v[26:27], v[2:3]
	v_pk_fma_f32 v[20:21], v[68:69], v[22:23], v[20:21]
	v_pk_fma_f32 v[2:3], v[50:51], v[28:29], v[2:3]
	v_pk_fma_f32 v[18:19], v[68:69], v[24:25], v[18:19]
	v_pk_fma_f32 v[2:3], v[52:53], v[30:31], v[2:3]
	v_pk_fma_f32 v[16:17], v[68:69], v[26:27], v[16:17]
	v_pk_fma_f32 v[2:3], v[54:55], v[32:33], v[2:3]
	v_pk_fma_f32 v[14:15], v[68:69], v[28:29], v[14:15]
	v_pk_fma_f32 v[2:3], v[56:57], v[34:35], v[2:3]
	v_pk_fma_f32 v[12:13], v[68:69], v[30:31], v[12:13]
	v_pk_fma_f32 v[2:3], v[58:59], v[36:37], v[2:3]
	v_pk_fma_f32 v[10:11], v[68:69], v[32:33], v[10:11]
	v_pk_fma_f32 v[2:3], v[60:61], v[38:39], v[2:3]
	v_pk_fma_f32 v[8:9], v[70:71], v[36:37], v[8:9]
	v_pk_fma_f32 v[2:3], v[62:63], v[40:41], v[2:3]
	v_pk_fma_f32 v[6:7], v[68:69], v[36:37], v[6:7]
	v_pk_fma_f32 v[2:3], v[64:65], v[42:43], v[2:3]
	v_pk_fma_f32 v[4:5], v[68:69], v[38:39], v[4:5]
	v_pk_fma_f32 v[2:3], v[66:67], v[44:45], v[2:3]
	v_pk_fma_f32 v[166:167], v[70:71], v[162:163], v[166:167]
	v_pk_fma_f32 v[2:3], v[68:69], v[120:121], v[2:3]
	v_pk_fma_f32 v[164:165], v[70:71], v[158:159], v[164:165]
	v_pk_fma_f32 v[160:161], v[70:71], v[22:23], v[160:161]
	v_pk_fma_f32 v[20:21], v[70:71], v[24:25], v[20:21]
	v_pk_fma_f32 v[18:19], v[70:71], v[26:27], v[18:19]
	v_pk_fma_f32 v[16:17], v[70:71], v[28:29], v[16:17]
	v_pk_fma_f32 v[14:15], v[70:71], v[30:31], v[14:15]
	v_pk_fma_f32 v[12:13], v[70:71], v[32:33], v[12:13]
	v_pk_fma_f32 v[10:11], v[70:71], v[34:35], v[10:11]
	v_pk_fma_f32 v[8:9], v[72:73], v[38:39], v[8:9]
	v_pk_fma_f32 v[6:7], v[70:71], v[38:39], v[6:7]
	v_pk_fma_f32 v[4:5], v[70:71], v[40:41], v[4:5]
	v_pk_fma_f32 v[2:3], v[70:71], v[122:123], v[2:3]
	v_pk_fma_f32 v[168:169], v[72:73], v[162:163], v[168:169]
	v_pk_fma_f32 v[166:167], v[72:73], v[158:159], v[166:167]
	v_pk_fma_f32 v[164:165], v[72:73], v[22:23], v[164:165]
	v_pk_fma_f32 v[160:161], v[72:73], v[24:25], v[160:161]
	v_pk_fma_f32 v[20:21], v[72:73], v[26:27], v[20:21]
	v_pk_fma_f32 v[18:19], v[72:73], v[28:29], v[18:19]
	v_pk_fma_f32 v[16:17], v[72:73], v[30:31], v[16:17]
	v_pk_fma_f32 v[14:15], v[72:73], v[32:33], v[14:15]
	v_pk_fma_f32 v[12:13], v[72:73], v[34:35], v[12:13]
	v_pk_fma_f32 v[10:11], v[72:73], v[36:37], v[10:11]
	v_pk_fma_f32 v[8:9], v[74:75], v[40:41], v[8:9]
	v_pk_fma_f32 v[6:7], v[72:73], v[40:41], v[6:7]
	v_pk_fma_f32 v[4:5], v[72:73], v[42:43], v[4:5]
	v_pk_fma_f32 v[2:3], v[72:73], v[124:125], v[2:3]
	v_pk_fma_f32 v[170:171], v[74:75], v[162:163], v[170:171]
	v_pk_fma_f32 v[168:169], v[74:75], v[158:159], v[168:169]
	v_pk_fma_f32 v[166:167], v[74:75], v[22:23], v[166:167]
	v_pk_fma_f32 v[164:165], v[74:75], v[24:25], v[164:165]
	v_pk_fma_f32 v[160:161], v[74:75], v[26:27], v[160:161]
	v_pk_fma_f32 v[20:21], v[74:75], v[28:29], v[20:21]
	v_pk_fma_f32 v[18:19], v[74:75], v[30:31], v[18:19]
	v_pk_fma_f32 v[16:17], v[74:75], v[32:33], v[16:17]
	v_pk_fma_f32 v[14:15], v[74:75], v[34:35], v[14:15]
	v_pk_fma_f32 v[12:13], v[74:75], v[36:37], v[12:13]
	v_pk_fma_f32 v[10:11], v[74:75], v[38:39], v[10:11]
	v_pk_fma_f32 v[8:9], v[76:77], v[42:43], v[8:9]
	v_pk_fma_f32 v[6:7], v[74:75], v[42:43], v[6:7]
	v_pk_fma_f32 v[4:5], v[74:75], v[44:45], v[4:5]
	v_pk_fma_f32 v[2:3], v[74:75], v[126:127], v[2:3]
	v_pk_fma_f32 v[172:173], v[76:77], v[162:163], v[172:173]
	v_pk_fma_f32 v[170:171], v[76:77], v[158:159], v[170:171]
	v_pk_fma_f32 v[168:169], v[76:77], v[22:23], v[168:169]
	v_pk_fma_f32 v[166:167], v[76:77], v[24:25], v[166:167]
	v_pk_fma_f32 v[164:165], v[76:77], v[26:27], v[164:165]
	v_pk_fma_f32 v[160:161], v[76:77], v[28:29], v[160:161]
	v_pk_fma_f32 v[20:21], v[76:77], v[30:31], v[20:21]
	v_pk_fma_f32 v[18:19], v[76:77], v[32:33], v[18:19]
	v_pk_fma_f32 v[16:17], v[76:77], v[34:35], v[16:17]
	v_pk_fma_f32 v[14:15], v[76:77], v[36:37], v[14:15]
	v_pk_fma_f32 v[12:13], v[76:77], v[38:39], v[12:13]
	v_pk_fma_f32 v[10:11], v[76:77], v[40:41], v[10:11]
	v_pk_fma_f32 v[8:9], v[78:79], v[44:45], v[8:9]
	v_pk_fma_f32 v[6:7], v[76:77], v[44:45], v[6:7]
	v_pk_fma_f32 v[4:5], v[76:77], v[120:121], v[4:5]
	v_pk_fma_f32 v[2:3], v[76:77], v[128:129], v[2:3]
	v_pk_fma_f32 v[174:175], v[78:79], v[162:163], v[174:175]
	v_pk_fma_f32 v[172:173], v[78:79], v[158:159], v[172:173]
	v_pk_fma_f32 v[170:171], v[78:79], v[22:23], v[170:171]
	v_pk_fma_f32 v[168:169], v[78:79], v[24:25], v[168:169]
	v_pk_fma_f32 v[166:167], v[78:79], v[26:27], v[166:167]
	v_pk_fma_f32 v[164:165], v[78:79], v[28:29], v[164:165]
	v_pk_fma_f32 v[160:161], v[78:79], v[30:31], v[160:161]
	v_pk_fma_f32 v[20:21], v[78:79], v[32:33], v[20:21]
	v_pk_fma_f32 v[18:19], v[78:79], v[34:35], v[18:19]
	v_pk_fma_f32 v[16:17], v[78:79], v[36:37], v[16:17]
	v_pk_fma_f32 v[14:15], v[78:79], v[38:39], v[14:15]
	v_pk_fma_f32 v[12:13], v[78:79], v[40:41], v[12:13]
	v_pk_fma_f32 v[10:11], v[78:79], v[42:43], v[10:11]
	v_pk_fma_f32 v[8:9], v[80:81], v[120:121], v[8:9]
	v_pk_fma_f32 v[6:7], v[78:79], v[120:121], v[6:7]
	v_pk_fma_f32 v[4:5], v[78:79], v[122:123], v[4:5]
	v_pk_fma_f32 v[2:3], v[78:79], v[130:131], v[2:3]
	v_pk_fma_f32 v[176:177], v[80:81], v[162:163], v[176:177]
	v_pk_fma_f32 v[174:175], v[80:81], v[158:159], v[174:175]
	v_pk_fma_f32 v[172:173], v[80:81], v[22:23], v[172:173]
	v_pk_fma_f32 v[170:171], v[80:81], v[24:25], v[170:171]
	v_pk_fma_f32 v[168:169], v[80:81], v[26:27], v[168:169]
	v_pk_fma_f32 v[166:167], v[80:81], v[28:29], v[166:167]
	v_pk_fma_f32 v[164:165], v[80:81], v[30:31], v[164:165]
	v_pk_fma_f32 v[160:161], v[80:81], v[32:33], v[160:161]
	v_pk_fma_f32 v[20:21], v[80:81], v[34:35], v[20:21]
	v_pk_fma_f32 v[18:19], v[80:81], v[36:37], v[18:19]
	v_pk_fma_f32 v[16:17], v[80:81], v[38:39], v[16:17]
	v_pk_fma_f32 v[14:15], v[80:81], v[40:41], v[14:15]
	v_pk_fma_f32 v[12:13], v[80:81], v[42:43], v[12:13]
	v_pk_fma_f32 v[10:11], v[80:81], v[44:45], v[10:11]
	v_pk_fma_f32 v[8:9], v[82:83], v[122:123], v[8:9]
	v_pk_fma_f32 v[6:7], v[80:81], v[122:123], v[6:7]
	v_pk_fma_f32 v[4:5], v[80:81], v[124:125], v[4:5]
	v_pk_fma_f32 v[2:3], v[80:81], v[134:135], v[2:3]
	v_pk_fma_f32 v[178:179], v[82:83], v[162:163], v[178:179]
	v_pk_fma_f32 v[176:177], v[82:83], v[158:159], v[176:177]
	v_pk_fma_f32 v[174:175], v[82:83], v[22:23], v[174:175]
	v_pk_fma_f32 v[172:173], v[82:83], v[24:25], v[172:173]
	v_pk_fma_f32 v[170:171], v[82:83], v[26:27], v[170:171]
	v_pk_fma_f32 v[168:169], v[82:83], v[28:29], v[168:169]
	v_pk_fma_f32 v[166:167], v[82:83], v[30:31], v[166:167]
	v_pk_fma_f32 v[164:165], v[82:83], v[32:33], v[164:165]
	v_pk_fma_f32 v[160:161], v[82:83], v[34:35], v[160:161]
	v_pk_fma_f32 v[20:21], v[82:83], v[36:37], v[20:21]
	v_pk_fma_f32 v[18:19], v[82:83], v[38:39], v[18:19]
	v_pk_fma_f32 v[16:17], v[82:83], v[40:41], v[16:17]
	v_pk_fma_f32 v[14:15], v[82:83], v[42:43], v[14:15]
	v_pk_fma_f32 v[12:13], v[82:83], v[44:45], v[12:13]
	v_pk_fma_f32 v[10:11], v[82:83], v[120:121], v[10:11]
	v_pk_fma_f32 v[8:9], v[84:85], v[124:125], v[8:9]
	v_pk_fma_f32 v[6:7], v[82:83], v[124:125], v[6:7]
	v_pk_fma_f32 v[4:5], v[82:83], v[126:127], v[4:5]
	v_pk_fma_f32 v[2:3], v[82:83], v[138:139], v[2:3]
	v_pk_fma_f32 v[180:181], v[84:85], v[162:163], v[180:181]
	v_pk_fma_f32 v[178:179], v[84:85], v[158:159], v[178:179]
	v_pk_fma_f32 v[176:177], v[84:85], v[22:23], v[176:177]
	v_pk_fma_f32 v[174:175], v[84:85], v[24:25], v[174:175]
	v_pk_fma_f32 v[172:173], v[84:85], v[26:27], v[172:173]
	v_pk_fma_f32 v[170:171], v[84:85], v[28:29], v[170:171]
	v_pk_fma_f32 v[168:169], v[84:85], v[30:31], v[168:169]
	v_pk_fma_f32 v[166:167], v[84:85], v[32:33], v[166:167]
	v_pk_fma_f32 v[164:165], v[84:85], v[34:35], v[164:165]
	v_pk_fma_f32 v[160:161], v[84:85], v[36:37], v[160:161]
	v_pk_fma_f32 v[20:21], v[84:85], v[38:39], v[20:21]
	v_pk_fma_f32 v[18:19], v[84:85], v[40:41], v[18:19]
	v_pk_fma_f32 v[16:17], v[84:85], v[42:43], v[16:17]
	v_pk_fma_f32 v[14:15], v[84:85], v[44:45], v[14:15]
	v_pk_fma_f32 v[12:13], v[84:85], v[120:121], v[12:13]
	v_pk_fma_f32 v[10:11], v[84:85], v[122:123], v[10:11]
	v_pk_fma_f32 v[8:9], v[86:87], v[126:127], v[8:9]
	v_pk_fma_f32 v[6:7], v[84:85], v[126:127], v[6:7]
	v_pk_fma_f32 v[4:5], v[84:85], v[128:129], v[4:5]
	v_pk_fma_f32 v[2:3], v[84:85], v[132:133], v[2:3]
	v_pk_fma_f32 v[182:183], v[86:87], v[162:163], v[182:183]
	v_pk_fma_f32 v[180:181], v[86:87], v[158:159], v[180:181]
	v_pk_fma_f32 v[178:179], v[86:87], v[22:23], v[178:179]
	v_pk_fma_f32 v[176:177], v[86:87], v[24:25], v[176:177]
	v_pk_fma_f32 v[174:175], v[86:87], v[26:27], v[174:175]
	v_pk_fma_f32 v[172:173], v[86:87], v[28:29], v[172:173]
	v_pk_fma_f32 v[170:171], v[86:87], v[30:31], v[170:171]
	v_pk_fma_f32 v[168:169], v[86:87], v[32:33], v[168:169]
	v_pk_fma_f32 v[166:167], v[86:87], v[34:35], v[166:167]
	v_pk_fma_f32 v[164:165], v[86:87], v[36:37], v[164:165]
	v_pk_fma_f32 v[160:161], v[86:87], v[38:39], v[160:161]
	v_pk_fma_f32 v[20:21], v[86:87], v[40:41], v[20:21]
	v_pk_fma_f32 v[18:19], v[86:87], v[42:43], v[18:19]
	v_pk_fma_f32 v[16:17], v[86:87], v[44:45], v[16:17]
	v_pk_fma_f32 v[14:15], v[86:87], v[120:121], v[14:15]
	v_pk_fma_f32 v[12:13], v[86:87], v[122:123], v[12:13]
	v_pk_fma_f32 v[10:11], v[86:87], v[124:125], v[10:11]
	v_pk_fma_f32 v[8:9], v[88:89], v[128:129], v[8:9]
	v_pk_fma_f32 v[6:7], v[86:87], v[128:129], v[6:7]
	v_pk_fma_f32 v[4:5], v[86:87], v[130:131], v[4:5]
	v_pk_fma_f32 v[2:3], v[86:87], v[136:137], v[2:3]
	v_pk_fma_f32 v[184:185], v[88:89], v[162:163], v[184:185]
	v_pk_fma_f32 v[182:183], v[88:89], v[158:159], v[182:183]
	v_pk_fma_f32 v[180:181], v[88:89], v[22:23], v[180:181]
	v_pk_fma_f32 v[178:179], v[88:89], v[24:25], v[178:179]
	v_pk_fma_f32 v[176:177], v[88:89], v[26:27], v[176:177]
	v_pk_fma_f32 v[174:175], v[88:89], v[28:29], v[174:175]
	v_pk_fma_f32 v[172:173], v[88:89], v[30:31], v[172:173]
	v_pk_fma_f32 v[170:171], v[88:89], v[32:33], v[170:171]
	v_pk_fma_f32 v[168:169], v[88:89], v[34:35], v[168:169]
	v_pk_fma_f32 v[166:167], v[88:89], v[36:37], v[166:167]
	v_pk_fma_f32 v[164:165], v[88:89], v[38:39], v[164:165]
	v_pk_fma_f32 v[160:161], v[88:89], v[40:41], v[160:161]
	v_pk_fma_f32 v[20:21], v[88:89], v[42:43], v[20:21]
	v_pk_fma_f32 v[18:19], v[88:89], v[44:45], v[18:19]
	v_pk_fma_f32 v[16:17], v[88:89], v[120:121], v[16:17]
	v_pk_fma_f32 v[14:15], v[88:89], v[122:123], v[14:15]
	v_pk_fma_f32 v[12:13], v[88:89], v[124:125], v[12:13]
	v_pk_fma_f32 v[10:11], v[88:89], v[126:127], v[10:11]
	v_pk_fma_f32 v[8:9], v[90:91], v[130:131], v[8:9]
	v_pk_fma_f32 v[6:7], v[88:89], v[130:131], v[6:7]
	v_pk_fma_f32 v[4:5], v[88:89], v[134:135], v[4:5]
	v_pk_fma_f32 v[2:3], v[88:89], v[140:141], v[2:3]
	v_pk_fma_f32 v[186:187], v[90:91], v[162:163], v[186:187]
	v_pk_fma_f32 v[184:185], v[90:91], v[158:159], v[184:185]
	v_pk_fma_f32 v[182:183], v[90:91], v[22:23], v[182:183]
	v_pk_fma_f32 v[180:181], v[90:91], v[24:25], v[180:181]
	v_pk_fma_f32 v[178:179], v[90:91], v[26:27], v[178:179]
	v_pk_fma_f32 v[176:177], v[90:91], v[28:29], v[176:177]
	v_pk_fma_f32 v[174:175], v[90:91], v[30:31], v[174:175]
	v_pk_fma_f32 v[172:173], v[90:91], v[32:33], v[172:173]
	v_pk_fma_f32 v[170:171], v[90:91], v[34:35], v[170:171]
	v_pk_fma_f32 v[168:169], v[90:91], v[36:37], v[168:169]
	v_pk_fma_f32 v[166:167], v[90:91], v[38:39], v[166:167]
	v_pk_fma_f32 v[164:165], v[90:91], v[40:41], v[164:165]
	v_pk_fma_f32 v[160:161], v[90:91], v[42:43], v[160:161]
	v_pk_fma_f32 v[20:21], v[90:91], v[44:45], v[20:21]
	v_pk_fma_f32 v[18:19], v[90:91], v[120:121], v[18:19]
	v_pk_fma_f32 v[16:17], v[90:91], v[122:123], v[16:17]
	v_pk_fma_f32 v[14:15], v[90:91], v[124:125], v[14:15]
	v_pk_fma_f32 v[12:13], v[90:91], v[126:127], v[12:13]
	v_pk_fma_f32 v[10:11], v[90:91], v[128:129], v[10:11]
	v_pk_fma_f32 v[8:9], v[92:93], v[134:135], v[8:9]
	v_pk_fma_f32 v[6:7], v[90:91], v[134:135], v[6:7]
	v_pk_fma_f32 v[4:5], v[90:91], v[138:139], v[4:5]
	v_pk_fma_f32 v[2:3], v[90:91], v[142:143], v[2:3]
	v_pk_fma_f32 v[212:213], v[92:93], v[162:163], v[212:213]
	v_pk_fma_f32 v[186:187], v[92:93], v[158:159], v[186:187]
	v_pk_fma_f32 v[184:185], v[92:93], v[22:23], v[184:185]
	v_pk_fma_f32 v[182:183], v[92:93], v[24:25], v[182:183]
	v_pk_fma_f32 v[180:181], v[92:93], v[26:27], v[180:181]
	v_pk_fma_f32 v[178:179], v[92:93], v[28:29], v[178:179]
	v_pk_fma_f32 v[176:177], v[92:93], v[30:31], v[176:177]
	v_pk_fma_f32 v[174:175], v[92:93], v[32:33], v[174:175]
	v_pk_fma_f32 v[172:173], v[92:93], v[34:35], v[172:173]
	v_pk_fma_f32 v[170:171], v[92:93], v[36:37], v[170:171]
	v_pk_fma_f32 v[168:169], v[92:93], v[38:39], v[168:169]
	v_pk_fma_f32 v[166:167], v[92:93], v[40:41], v[166:167]
	v_pk_fma_f32 v[164:165], v[92:93], v[42:43], v[164:165]
	v_pk_fma_f32 v[160:161], v[92:93], v[44:45], v[160:161]
	v_pk_fma_f32 v[20:21], v[92:93], v[120:121], v[20:21]
	v_pk_fma_f32 v[18:19], v[92:93], v[122:123], v[18:19]
	v_pk_fma_f32 v[16:17], v[92:93], v[124:125], v[16:17]
	v_pk_fma_f32 v[14:15], v[92:93], v[126:127], v[14:15]
	v_pk_fma_f32 v[12:13], v[92:93], v[128:129], v[12:13]
	v_pk_fma_f32 v[10:11], v[92:93], v[130:131], v[10:11]
	v_pk_fma_f32 v[8:9], v[94:95], v[138:139], v[8:9]
	v_pk_fma_f32 v[6:7], v[92:93], v[138:139], v[6:7]
	v_pk_fma_f32 v[4:5], v[92:93], v[132:133], v[4:5]
	v_pk_fma_f32 v[2:3], v[92:93], v[144:145], v[2:3]
	v_pk_fma_f32 v[214:215], v[94:95], v[162:163], v[214:215]
	v_pk_fma_f32 v[212:213], v[94:95], v[158:159], v[212:213]
	v_pk_fma_f32 v[186:187], v[94:95], v[22:23], v[186:187]
	v_pk_fma_f32 v[184:185], v[94:95], v[24:25], v[184:185]
	v_pk_fma_f32 v[182:183], v[94:95], v[26:27], v[182:183]
	v_pk_fma_f32 v[180:181], v[94:95], v[28:29], v[180:181]
	v_pk_fma_f32 v[178:179], v[94:95], v[30:31], v[178:179]
	v_pk_fma_f32 v[176:177], v[94:95], v[32:33], v[176:177]
	v_pk_fma_f32 v[174:175], v[94:95], v[34:35], v[174:175]
	v_pk_fma_f32 v[172:173], v[94:95], v[36:37], v[172:173]
	v_pk_fma_f32 v[170:171], v[94:95], v[38:39], v[170:171]
	v_pk_fma_f32 v[168:169], v[94:95], v[40:41], v[168:169]
	v_pk_fma_f32 v[166:167], v[94:95], v[42:43], v[166:167]
	v_pk_fma_f32 v[164:165], v[94:95], v[44:45], v[164:165]
	v_pk_fma_f32 v[160:161], v[94:95], v[120:121], v[160:161]
	v_pk_fma_f32 v[20:21], v[94:95], v[122:123], v[20:21]
	v_pk_fma_f32 v[18:19], v[94:95], v[124:125], v[18:19]
	v_pk_fma_f32 v[16:17], v[94:95], v[126:127], v[16:17]
	v_pk_fma_f32 v[14:15], v[94:95], v[128:129], v[14:15]
	v_pk_fma_f32 v[12:13], v[94:95], v[130:131], v[12:13]
	v_pk_fma_f32 v[10:11], v[94:95], v[134:135], v[10:11]
	v_pk_fma_f32 v[8:9], v[96:97], v[132:133], v[8:9]
	v_pk_fma_f32 v[6:7], v[94:95], v[132:133], v[6:7]
	v_pk_fma_f32 v[4:5], v[94:95], v[136:137], v[4:5]
	v_pk_fma_f32 v[2:3], v[94:95], v[146:147], v[2:3]
	v_pk_fma_f32 v[216:217], v[96:97], v[162:163], v[216:217]
	v_pk_fma_f32 v[214:215], v[96:97], v[158:159], v[214:215]
	v_pk_fma_f32 v[212:213], v[96:97], v[22:23], v[212:213]
	v_pk_fma_f32 v[186:187], v[96:97], v[24:25], v[186:187]
	v_pk_fma_f32 v[184:185], v[96:97], v[26:27], v[184:185]
	v_pk_fma_f32 v[182:183], v[96:97], v[28:29], v[182:183]
	v_pk_fma_f32 v[180:181], v[96:97], v[30:31], v[180:181]
	v_pk_fma_f32 v[178:179], v[96:97], v[32:33], v[178:179]
	v_pk_fma_f32 v[176:177], v[96:97], v[34:35], v[176:177]
	v_pk_fma_f32 v[174:175], v[96:97], v[36:37], v[174:175]
	v_pk_fma_f32 v[172:173], v[96:97], v[38:39], v[172:173]
	v_pk_fma_f32 v[170:171], v[96:97], v[40:41], v[170:171]
	v_pk_fma_f32 v[168:169], v[96:97], v[42:43], v[168:169]
	v_pk_fma_f32 v[166:167], v[96:97], v[44:45], v[166:167]
	v_pk_fma_f32 v[164:165], v[96:97], v[120:121], v[164:165]
	v_pk_fma_f32 v[160:161], v[96:97], v[122:123], v[160:161]
	v_pk_fma_f32 v[20:21], v[96:97], v[124:125], v[20:21]
	v_pk_fma_f32 v[18:19], v[96:97], v[126:127], v[18:19]
	v_pk_fma_f32 v[16:17], v[96:97], v[128:129], v[16:17]
	v_pk_fma_f32 v[14:15], v[96:97], v[130:131], v[14:15]
	v_pk_fma_f32 v[12:13], v[96:97], v[134:135], v[12:13]
	v_pk_fma_f32 v[10:11], v[96:97], v[138:139], v[10:11]
	v_pk_fma_f32 v[8:9], v[98:99], v[136:137], v[8:9]
	v_pk_fma_f32 v[6:7], v[96:97], v[136:137], v[6:7]
	v_pk_fma_f32 v[4:5], v[96:97], v[140:141], v[4:5]
	v_pk_fma_f32 v[2:3], v[96:97], v[148:149], v[2:3]
	v_pk_fma_f32 v[220:221], v[98:99], v[162:163], v[220:221]
	v_pk_fma_f32 v[216:217], v[98:99], v[158:159], v[216:217]
	v_pk_fma_f32 v[214:215], v[98:99], v[22:23], v[214:215]
	v_pk_fma_f32 v[212:213], v[98:99], v[24:25], v[212:213]
	v_pk_fma_f32 v[186:187], v[98:99], v[26:27], v[186:187]
	v_pk_fma_f32 v[184:185], v[98:99], v[28:29], v[184:185]
	v_pk_fma_f32 v[182:183], v[98:99], v[30:31], v[182:183]
	v_pk_fma_f32 v[180:181], v[98:99], v[32:33], v[180:181]
	v_pk_fma_f32 v[178:179], v[98:99], v[34:35], v[178:179]
	v_pk_fma_f32 v[176:177], v[98:99], v[36:37], v[176:177]
	v_pk_fma_f32 v[174:175], v[98:99], v[38:39], v[174:175]
	v_pk_fma_f32 v[172:173], v[98:99], v[40:41], v[172:173]
	v_pk_fma_f32 v[170:171], v[98:99], v[42:43], v[170:171]
	v_pk_fma_f32 v[168:169], v[98:99], v[44:45], v[168:169]
	v_pk_fma_f32 v[166:167], v[98:99], v[120:121], v[166:167]
	v_pk_fma_f32 v[164:165], v[98:99], v[122:123], v[164:165]
	v_pk_fma_f32 v[160:161], v[98:99], v[124:125], v[160:161]
	v_pk_fma_f32 v[20:21], v[98:99], v[126:127], v[20:21]
	v_pk_fma_f32 v[18:19], v[98:99], v[128:129], v[18:19]
	v_pk_fma_f32 v[16:17], v[98:99], v[130:131], v[16:17]
	v_pk_fma_f32 v[14:15], v[98:99], v[134:135], v[14:15]
	v_pk_fma_f32 v[12:13], v[98:99], v[138:139], v[12:13]
	v_pk_fma_f32 v[10:11], v[98:99], v[132:133], v[10:11]
	v_pk_fma_f32 v[8:9], v[100:101], v[140:141], v[8:9]
	v_pk_fma_f32 v[6:7], v[98:99], v[140:141], v[6:7]
	v_pk_fma_f32 v[4:5], v[98:99], v[142:143], v[4:5]
	v_pk_fma_f32 v[2:3], v[98:99], v[150:151], v[2:3]
	v_pk_fma_f32 v[222:223], v[100:101], v[162:163], v[222:223]
	v_pk_fma_f32 v[220:221], v[100:101], v[158:159], v[220:221]
	v_pk_fma_f32 v[216:217], v[100:101], v[22:23], v[216:217]
	v_pk_fma_f32 v[214:215], v[100:101], v[24:25], v[214:215]
	v_pk_fma_f32 v[212:213], v[100:101], v[26:27], v[212:213]
	v_pk_fma_f32 v[186:187], v[100:101], v[28:29], v[186:187]
	v_pk_fma_f32 v[184:185], v[100:101], v[30:31], v[184:185]
	v_pk_fma_f32 v[182:183], v[100:101], v[32:33], v[182:183]
	v_pk_fma_f32 v[180:181], v[100:101], v[34:35], v[180:181]
	v_pk_fma_f32 v[178:179], v[100:101], v[36:37], v[178:179]
	v_pk_fma_f32 v[176:177], v[100:101], v[38:39], v[176:177]
	v_pk_fma_f32 v[174:175], v[100:101], v[40:41], v[174:175]
	v_pk_fma_f32 v[172:173], v[100:101], v[42:43], v[172:173]
	v_pk_fma_f32 v[170:171], v[100:101], v[44:45], v[170:171]
	v_pk_fma_f32 v[168:169], v[100:101], v[120:121], v[168:169]
	v_pk_fma_f32 v[166:167], v[100:101], v[122:123], v[166:167]
	v_pk_fma_f32 v[164:165], v[100:101], v[124:125], v[164:165]
	v_pk_fma_f32 v[160:161], v[100:101], v[126:127], v[160:161]
	v_pk_fma_f32 v[20:21], v[100:101], v[128:129], v[20:21]
	v_pk_fma_f32 v[18:19], v[100:101], v[130:131], v[18:19]
	v_pk_fma_f32 v[16:17], v[100:101], v[134:135], v[16:17]
	v_pk_fma_f32 v[14:15], v[100:101], v[138:139], v[14:15]
	v_pk_fma_f32 v[12:13], v[100:101], v[132:133], v[12:13]
	v_pk_fma_f32 v[10:11], v[100:101], v[136:137], v[10:11]
	v_pk_fma_f32 v[8:9], v[102:103], v[142:143], v[8:9]
	v_pk_fma_f32 v[6:7], v[100:101], v[142:143], v[6:7]
	v_pk_fma_f32 v[4:5], v[100:101], v[144:145], v[4:5]
	v_pk_fma_f32 v[2:3], v[100:101], v[152:153], v[2:3]
	s_waitcnt vmcnt(0)
	v_lshlrev_b32_e32 v156, 16, v157
	v_and_b32_e32 v157, 0xffff0000, v157
	v_pk_fma_f32 v[224:225], v[102:103], v[162:163], v[224:225]
	v_pk_fma_f32 v[222:223], v[102:103], v[158:159], v[222:223]
	v_pk_fma_f32 v[220:221], v[102:103], v[22:23], v[220:221]
	v_pk_fma_f32 v[216:217], v[102:103], v[24:25], v[216:217]
	v_pk_fma_f32 v[214:215], v[102:103], v[26:27], v[214:215]
	v_pk_fma_f32 v[212:213], v[102:103], v[28:29], v[212:213]
	v_pk_fma_f32 v[186:187], v[102:103], v[30:31], v[186:187]
	v_pk_fma_f32 v[184:185], v[102:103], v[32:33], v[184:185]
	v_pk_fma_f32 v[182:183], v[102:103], v[34:35], v[182:183]
	v_pk_fma_f32 v[180:181], v[102:103], v[36:37], v[180:181]
	v_pk_fma_f32 v[178:179], v[102:103], v[38:39], v[178:179]
	v_pk_fma_f32 v[176:177], v[102:103], v[40:41], v[176:177]
	v_pk_fma_f32 v[174:175], v[102:103], v[42:43], v[174:175]
	v_pk_fma_f32 v[172:173], v[102:103], v[44:45], v[172:173]
	v_pk_fma_f32 v[170:171], v[102:103], v[120:121], v[170:171]
	v_pk_fma_f32 v[168:169], v[102:103], v[122:123], v[168:169]
	v_pk_fma_f32 v[166:167], v[102:103], v[124:125], v[166:167]
	v_pk_fma_f32 v[164:165], v[102:103], v[126:127], v[164:165]
	v_pk_fma_f32 v[160:161], v[102:103], v[128:129], v[160:161]
	v_pk_fma_f32 v[20:21], v[102:103], v[130:131], v[20:21]
	v_pk_fma_f32 v[18:19], v[102:103], v[134:135], v[18:19]
	v_pk_fma_f32 v[16:17], v[102:103], v[138:139], v[16:17]
	v_pk_fma_f32 v[14:15], v[102:103], v[132:133], v[14:15]
	v_pk_fma_f32 v[12:13], v[102:103], v[136:137], v[12:13]
	v_pk_fma_f32 v[10:11], v[102:103], v[140:141], v[10:11]
	v_pk_fma_f32 v[8:9], v[104:105], v[144:145], v[8:9]
	v_pk_fma_f32 v[6:7], v[102:103], v[144:145], v[6:7]
	v_pk_fma_f32 v[4:5], v[102:103], v[146:147], v[4:5]
	v_pk_fma_f32 v[2:3], v[102:103], v[154:155], v[2:3]
	v_pk_fma_f32 v[224:225], v[104:105], v[158:159], v[224:225]
	v_pk_fma_f32 v[222:223], v[104:105], v[22:23], v[222:223]
	v_pk_fma_f32 v[220:221], v[104:105], v[24:25], v[220:221]
	v_pk_fma_f32 v[216:217], v[104:105], v[26:27], v[216:217]
	v_pk_fma_f32 v[214:215], v[104:105], v[28:29], v[214:215]
	v_pk_fma_f32 v[212:213], v[104:105], v[30:31], v[212:213]
	v_pk_fma_f32 v[186:187], v[104:105], v[32:33], v[186:187]
	v_pk_fma_f32 v[184:185], v[104:105], v[34:35], v[184:185]
	v_pk_fma_f32 v[182:183], v[104:105], v[36:37], v[182:183]
	v_pk_fma_f32 v[180:181], v[104:105], v[38:39], v[180:181]
	v_pk_fma_f32 v[178:179], v[104:105], v[40:41], v[178:179]
	v_pk_fma_f32 v[176:177], v[104:105], v[42:43], v[176:177]
	v_pk_fma_f32 v[174:175], v[104:105], v[44:45], v[174:175]
	v_pk_fma_f32 v[172:173], v[104:105], v[120:121], v[172:173]
	v_pk_fma_f32 v[170:171], v[104:105], v[122:123], v[170:171]
	v_pk_fma_f32 v[168:169], v[104:105], v[124:125], v[168:169]
	v_pk_fma_f32 v[166:167], v[104:105], v[126:127], v[166:167]
	v_pk_fma_f32 v[164:165], v[104:105], v[128:129], v[164:165]
	v_pk_fma_f32 v[160:161], v[104:105], v[130:131], v[160:161]
	v_pk_fma_f32 v[20:21], v[104:105], v[134:135], v[20:21]
	v_pk_fma_f32 v[18:19], v[104:105], v[138:139], v[18:19]
	v_pk_fma_f32 v[16:17], v[104:105], v[132:133], v[16:17]
	v_pk_fma_f32 v[14:15], v[104:105], v[136:137], v[14:15]
	v_pk_fma_f32 v[12:13], v[104:105], v[140:141], v[12:13]
	v_pk_fma_f32 v[10:11], v[104:105], v[142:143], v[10:11]
	ds_write_b64 v198, v[8:9]
	v_pk_fma_f32 v[6:7], v[104:105], v[146:147], v[6:7]
	v_pk_fma_f32 v[4:5], v[104:105], v[148:149], v[4:5]
	v_pk_fma_f32 v[2:3], v[104:105], v[156:157], v[2:3]
	v_add_u32_e32 v8, s8, v112
	ds_write2st64_b64 v1, v[224:225], v[222:223] offset1:8
	ds_write2st64_b64 v1, v[220:221], v[216:217] offset0:16 offset1:24
	ds_write2st64_b64 v1, v[214:215], v[212:213] offset0:32 offset1:40
	ds_write2st64_b64 v1, v[186:187], v[184:185] offset0:48 offset1:56
	ds_write2st64_b64 v1, v[182:183], v[180:181] offset0:64 offset1:72
	ds_write2st64_b64 v1, v[178:179], v[176:177] offset0:80 offset1:88
	ds_write2st64_b64 v1, v[174:175], v[172:173] offset0:96 offset1:104
	ds_write2st64_b64 v1, v[170:171], v[168:169] offset0:112 offset1:120
	ds_write_b64 v189, v[166:167]
	ds_write_b64 v190, v[164:165]
	ds_write_b64 v191, v[160:161]
	ds_write_b64 v192, v[20:21]
	ds_write_b64 v193, v[18:19]
	ds_write_b64 v194, v[16:17]
	ds_write_b64 v195, v[14:15]
	ds_write_b64 v196, v[12:13]
	ds_write_b64 v197, v[10:11]
	ds_write_b64 v199, v[6:7]
	ds_write_b64 v200, v[4:5]
	ds_write_b64 v204, v[2:3]
	s_waitcnt lgkmcnt(0)
	s_barrier
	ds_read_b128 v[42:45], v8
	ds_read_b128 v[124:127], v8 offset:1024
	ds_read_b128 v[32:35], v8 offset:2048
	ds_read_b128 v[38:41], v8 offset:3072
	s_add_i32 s0, s3, s4
	s_waitcnt lgkmcnt(3)
	v_mov_b32_e32 v2, v43
	v_mov_b32_e32 v3, v44
	v_mov_b32_e32 v4, v42
	v_mov_b32_e32 v5, v45
	v_pk_add_f32 v[2:3], v[2:3], v[4:5]
	s_waitcnt lgkmcnt(2)
	v_mov_b32_e32 v4, v125
	v_mov_b32_e32 v5, v126
	v_mov_b32_e32 v6, v124
	v_mov_b32_e32 v7, v127
	v_pk_add_f32 v[4:5], v[4:5], v[6:7]
	v_add_f32_e32 v2, v2, v3
	v_pk_add_f32 v[4:5], v[4:5], v[4:5] op_sel:[0,1] op_sel_hi:[1,0]
	v_add_f32_e32 v2, 0, v2
	s_waitcnt lgkmcnt(1)
	v_add_f32_e32 v6, v32, v33
	v_add_f32_e32 v8, v34, v35
	s_waitcnt lgkmcnt(0)
	v_mov_b32_e32 v3, v38
	v_mov_b32_e32 v5, v39
	v_mov_b32_e32 v7, v40
	v_mov_b32_e32 v9, v41
	v_pk_add_f32 v[2:3], v[2:3], v[4:5]
	v_pk_add_f32 v[4:5], v[6:7], v[8:9]
	s_sub_i32 s6, s0, 31
	v_pk_add_f32 v[2:3], v[2:3], v[4:5]
	s_ashr_i32 s7, s6, 31
	v_add_f32_e32 v2, v2, v3
	s_nop 1
	v_mov_b32_dpp v3, v2 quad_perm:[1,0,3,2] row_mask:0xf bank_mask:0xf
	s_lshl_b64 s[6:7], s[6:7], 12
	s_add_i32 s14, s14, s34
	s_add_i32 s4, s4, s12
	s_waitcnt lgkmcnt(0)
	v_add_f32_e32 v2, v2, v3
	s_nop 1
	v_mov_b32_dpp v3, v2 quad_perm:[2,3,0,1] row_mask:0xf bank_mask:0xf
	s_waitcnt lgkmcnt(0)
	v_add_f32_e32 v2, v2, v3
	s_nop 1
	v_mov_b32_dpp v3, v2 row_half_mirror row_mask:0xf bank_mask:0xf
	s_waitcnt lgkmcnt(0)
	v_add_f32_e32 v2, v2, v3
	s_nop 1
	v_mov_b32_dpp v3, v2 row_mirror row_mask:0xf bank_mask:0xf
	s_waitcnt lgkmcnt(0)
	v_add_f32_e32 v2, v2, v3
	ds_bpermute_b32 v3, v209, v2
	s_waitcnt lgkmcnt(0)
	v_add_f32_e32 v10, v2, v3
	global_load_dwordx4 v[18:21], v[114:115], off
	global_load_dwordx4 v[2:5], v[114:115], off offset:1024
	global_load_dwordx4 v[22:25], v[116:117], off
	global_load_dwordx4 v[6:9], v[116:117], off offset:1024
	ds_bpermute_b32 v11, v210, v10
	s_waitcnt lgkmcnt(0)
	v_add_f32_e32 v26, v10, v11
	v_fmamk_f32 v37, v26, 0xba800000, v43
	v_fmamk_f32 v36, v26, 0xba800000, v42
	v_fmamk_f32 v45, v26, 0xba800000, v45
	v_fmac_f32_e32 v44, 0xba800000, v26
	v_pk_mul_f32 v[10:11], v[44:45], v[44:45]
	v_pk_mul_f32 v[12:13], v[36:37], v[36:37]
	v_fmamk_f32 v43, v26, 0xba800000, v125
	v_pk_mov_b32 v[14:15], v[12:13], v[10:11] op_sel:[1,0]
	v_mov_b32_e32 v13, v11
	v_pk_add_f32 v[10:11], v[14:15], v[12:13]
	v_fmamk_f32 v42, v26, 0xba800000, v124
	v_fmamk_f32 v127, v26, 0xba800000, v127
	v_fmac_f32_e32 v126, 0xba800000, v26
	v_pk_add_f32 v[10:11], v[10:11], v[10:11] op_sel_hi:[0,1]
	v_pk_mul_f32 v[12:13], v[126:127], v[126:127]
	v_pk_mul_f32 v[14:15], v[42:43], v[42:43]
	v_fmamk_f32 v130, v26, 0xba800000, v32
	v_pk_mov_b32 v[16:17], v[14:15], v[12:13] op_sel:[1,0]
	v_mov_b32_e32 v15, v13
	v_fmamk_f32 v131, v26, 0xba800000, v33
	v_fmac_f32_e32 v34, 0xba800000, v26
	v_mul_f32_e32 v10, v130, v130
	v_pk_add_f32 v[12:13], v[16:17], v[14:15]
	v_fmamk_f32 v35, v26, 0xba800000, v35
	v_pk_fma_f32 v[14:15], v[130:131], v[130:131], v[10:11] op_sel_hi:[1,1,0]
	v_mul_f32_e32 v10, v34, v34
	v_pk_add_f32 v[12:13], v[12:13], v[12:13] op_sel_hi:[0,1]
	v_pk_fma_f32 v[16:17], v[34:35], v[34:35], v[10:11] op_sel_hi:[1,1,0]
	v_fmamk_f32 v121, v26, 0xba800000, v41
	v_fmamk_f32 v120, v26, 0xba800000, v40
	v_fmamk_f32 v39, v26, 0xba800000, v39
	v_fmac_f32_e32 v38, 0xba800000, v26
	v_mul_f32_e32 v14, v38, v38
	v_mul_f32_e32 v16, v39, v39
	v_mul_f32_e32 v10, v120, v120
	v_mul_f32_e32 v12, v121, v121
	v_pk_add_f32 v[14:15], v[14:15], v[16:17]
	v_pk_add_f32 v[10:11], v[10:11], v[12:13]
	global_load_dwordx4 v[26:29], v[114:115], off offset:2048
	global_load_dwordx4 v[30:33], v[116:117], off offset:2048
	v_pk_add_f32 v[10:11], v[14:15], v[10:11]
	s_nop 0
	v_add_f32_e32 v10, v10, v11
	s_nop 1
	v_mov_b32_dpp v11, v10 quad_perm:[1,0,3,2] row_mask:0xf bank_mask:0xf
	s_waitcnt lgkmcnt(0)
	v_add_f32_e32 v10, v10, v11
	s_nop 1
	v_mov_b32_dpp v11, v10 quad_perm:[2,3,0,1] row_mask:0xf bank_mask:0xf
	s_waitcnt lgkmcnt(0)
	v_add_f32_e32 v10, v10, v11
	s_nop 1
	v_mov_b32_dpp v11, v10 row_half_mirror row_mask:0xf bank_mask:0xf
	s_waitcnt lgkmcnt(0)
	v_add_f32_e32 v10, v10, v11
	s_nop 1
	v_mov_b32_dpp v11, v10 row_mirror row_mask:0xf bank_mask:0xf
	s_waitcnt lgkmcnt(0)
	v_add_f32_e32 v10, v10, v11
	ds_bpermute_b32 v11, v209, v10
	s_waitcnt lgkmcnt(0)
	v_add_f32_e32 v10, v10, v11
	ds_bpermute_b32 v11, v210, v10
	s_waitcnt lgkmcnt(0)
	v_add_f32_e32 v10, v10, v11
	v_fmamk_f32 v10, v10, 0x3a800000, v211
	v_mul_f32_e32 v11, 0x4b800000, v10
	v_cmp_gt_f32_e32 vcc, s13, v10
	s_nop 1
	v_cndmask_b32_e32 v10, v10, v11, vcc
	v_rsq_f32_e32 v40, v10
	global_load_dwordx4 v[10:13], v[114:115], off offset:3072
	global_load_dwordx4 v[14:17], v[116:117], off offset:3072
	v_mul_f32_e32 v41, 0x45800000, v40
	v_cndmask_b32_e32 v122, v40, v41, vcc
	v_pk_mul_f32 v[36:37], v[36:37], v[122:123] op_sel_hi:[1,0]
	s_waitcnt vmcnt(5)
	v_pk_fma_f32 v[36:37], v[18:19], v[36:37], v[22:23]
	s_nop 0
	v_mul_f32_e32 v40, 0xbfb8aa3b, v36
	v_exp_f32_e32 v40, v40
	s_nop 0
	v_add_f32_e32 v40, 1.0, v40
	v_rcp_f32_e32 v123, v40
	v_mul_f32_e32 v40, 0xbfb8aa3b, v37
	v_exp_f32_e32 v124, v40
	v_pk_mul_f32 v[40:41], v[44:45], v[122:123] op_sel_hi:[1,0]
	s_nop 0
	v_pk_fma_f32 v[40:41], v[20:21], v[40:41], v[24:25]
	v_mul_f32_e32 v36, v36, v123
	v_mul_f32_e32 v45, 0xbfb8aa3b, v40
	v_mul_f32_e32 v123, 0xbfb8aa3b, v41
	v_exp_f32_e32 v45, v45
	v_exp_f32_e32 v123, v123
	v_add_f32_e32 v44, 1.0, v124
	v_rcp_f32_e32 v44, v44
	v_add_f32_e32 v45, 1.0, v45
	v_add_f32_e32 v123, 1.0, v123
	v_rcp_f32_e32 v45, v45
	v_rcp_f32_e32 v123, v123
	v_mul_f32_e32 v37, v37, v44
	v_cvt_pk_bf16_f32 v36, v36, v37
	v_mul_f32_e32 v37, v40, v45
	v_mul_f32_e32 v44, v41, v123
	v_pk_mul_f32 v[40:41], v[42:43], v[122:123] op_sel_hi:[1,0]
	v_lshl_add_u64 v[124:125], v[118:119], 0, s[6:7]
	s_waitcnt vmcnt(4)
	v_pk_fma_f32 v[40:41], v[2:3], v[40:41], v[6:7]
	v_cvt_pk_bf16_f32 v37, v37, v44
	global_store_dwordx2 v[124:125], v[36:37], off
	v_mul_f32_e32 v42, 0xbfb8aa3b, v40
	v_exp_f32_e32 v42, v42
	s_sub_i32 s6, s0, 30
	s_ashr_i32 s7, s6, 31
	s_lshl_b64 s[6:7], s[6:7], 12
	v_add_f32_e32 v36, 1.0, v42
	v_rcp_f32_e32 v42, v36
	v_mul_f32_e32 v36, 0xbfb8aa3b, v41
	v_exp_f32_e32 v43, v36
	v_pk_mul_f32 v[36:37], v[126:127], v[122:123] op_sel_hi:[1,0]
	v_mul_f32_e32 v40, v40, v42
	v_pk_fma_f32 v[36:37], v[4:5], v[36:37], v[8:9]
	v_add_f32_e32 v42, 1.0, v43
	v_mul_f32_e32 v43, 0xbfb8aa3b, v36
	v_mul_f32_e32 v44, 0xbfb8aa3b, v37
	v_exp_f32_e32 v43, v43
	v_exp_f32_e32 v44, v44
	v_rcp_f32_e32 v42, v42
	v_add_u32_e32 v123, s9, v113
	v_add_f32_e32 v43, 1.0, v43
	v_add_f32_e32 v44, 1.0, v44
	v_rcp_f32_e32 v43, v43
	v_rcp_f32_e32 v44, v44
	ds_read_b128 v[126:129], v123
	v_mul_f32_e32 v41, v41, v42
	v_mul_f32_e32 v36, v36, v43
	v_mul_f32_e32 v37, v37, v44
	v_cvt_pk_bf16_f32 v40, v40, v41
	v_cvt_pk_bf16_f32 v41, v36, v37
	v_pk_mul_f32 v[36:37], v[130:131], v[122:123] op_sel_hi:[1,0]
	v_pk_mul_f32 v[44:45], v[34:35], v[122:123] op_sel_hi:[1,0]
	s_waitcnt vmcnt(3)
	v_pk_fma_f32 v[134:135], v[26:27], v[36:37], v[30:31]
	ds_read_b128 v[130:133], v123 offset:1024
	s_waitcnt lgkmcnt(1)
	v_mov_b32_e32 v34, v127
	v_mov_b32_e32 v35, v128
	v_mov_b32_e32 v36, v126
	v_mov_b32_e32 v37, v129
	v_pk_add_f32 v[34:35], v[34:35], v[36:37]
	global_store_dwordx2 v[124:125], v[40:41], off offset:512
	v_add_f32_e32 v34, v34, v35
	v_add_f32_e32 v136, 0, v34
	ds_read_b128 v[40:43], v123 offset:2048
	ds_read_b128 v[34:37], v123 offset:3072
	s_waitcnt lgkmcnt(2)
	v_mov_b32_e32 v138, v131
	v_mov_b32_e32 v139, v132
	v_mov_b32_e32 v140, v130
	v_mov_b32_e32 v141, v133
	v_pk_add_f32 v[138:139], v[138:139], v[140:141]
	s_waitcnt lgkmcnt(1)
	v_add_f32_e32 v140, v40, v41
	v_pk_add_f32 v[138:139], v[138:139], v[138:139] op_sel:[0,1] op_sel_hi:[1,0]
	v_add_f32_e32 v142, v42, v43
	s_waitcnt lgkmcnt(0)
	v_mov_b32_e32 v137, v34
	v_mov_b32_e32 v139, v35
	v_mov_b32_e32 v141, v36
	v_mov_b32_e32 v143, v37
	v_pk_add_f32 v[136:137], v[136:137], v[138:139]
	v_pk_add_f32 v[138:139], v[140:141], v[142:143]
	v_pk_fma_f32 v[44:45], v[28:29], v[44:45], v[32:33]
	v_pk_add_f32 v[136:137], v[136:137], v[138:139]
	v_mul_f32_e32 v138, 0xbfb8aa3b, v135
	v_add_f32_e32 v123, v136, v137
	s_nop 1
	v_mov_b32_dpp v136, v123 quad_perm:[1,0,3,2] row_mask:0xf bank_mask:0xf
	v_mul_f32_e32 v137, 0xbfb8aa3b, v134
	v_exp_f32_e32 v137, v137
	v_exp_f32_e32 v138, v138
	s_waitcnt lgkmcnt(0)
	v_add_f32_e32 v123, v123, v136
	s_nop 1
	v_mov_b32_dpp v136, v123 quad_perm:[2,3,0,1] row_mask:0xf bank_mask:0xf
	v_add_f32_e32 v137, 1.0, v137
	v_add_f32_e32 v138, 1.0, v138
	v_rcp_f32_e32 v137, v137
	v_rcp_f32_e32 v138, v138
	s_waitcnt lgkmcnt(0)
	v_add_f32_e32 v123, v123, v136
	s_nop 1
	v_mov_b32_dpp v136, v123 row_half_mirror row_mask:0xf bank_mask:0xf
	v_mul_f32_e32 v134, v134, v137
	v_mul_f32_e32 v135, v135, v138
	v_cvt_pk_bf16_f32 v134, v134, v135
	v_mul_f32_e32 v137, 0xbfb8aa3b, v45
	s_waitcnt lgkmcnt(0)
	v_add_f32_e32 v123, v123, v136
	s_nop 1
	v_mov_b32_dpp v135, v123 row_mirror row_mask:0xf bank_mask:0xf
	v_mul_f32_e32 v136, 0xbfb8aa3b, v44
	v_exp_f32_e32 v136, v136
	v_exp_f32_e32 v137, v137
	s_waitcnt lgkmcnt(0)
	v_add_f32_e32 v123, v123, v135
	ds_bpermute_b32 v135, v209, v123
	v_add_f32_e32 v136, 1.0, v136
	v_add_f32_e32 v137, 1.0, v137
	v_rcp_f32_e32 v136, v136
	v_rcp_f32_e32 v137, v137
	s_waitcnt lgkmcnt(0)
	v_add_f32_e32 v123, v123, v135
	ds_bpermute_b32 v138, v210, v123
	v_mul_f32_e32 v44, v44, v136
	v_mul_f32_e32 v45, v45, v137
	v_cvt_pk_bf16_f32 v135, v44, v45
	global_store_dwordx2 v[124:125], v[134:135], off offset:1024
	s_waitcnt lgkmcnt(0)
	v_add_f32_e32 v123, v123, v138
	v_fmamk_f32 v127, v123, 0xba800000, v127
	v_fmamk_f32 v126, v123, 0xba800000, v126
	v_fmamk_f32 v129, v123, 0xba800000, v129
	v_fmac_f32_e32 v128, 0xba800000, v123
	v_pk_mul_f32 v[44:45], v[128:129], v[128:129]
	v_pk_mul_f32 v[134:135], v[126:127], v[126:127]
	v_fmamk_f32 v131, v123, 0xba800000, v131
	v_pk_mov_b32 v[136:137], v[134:135], v[44:45] op_sel:[1,0]
	v_mov_b32_e32 v135, v45
	v_pk_add_f32 v[44:45], v[136:137], v[134:135]
	v_fmamk_f32 v130, v123, 0xba800000, v130
	v_fmamk_f32 v133, v123, 0xba800000, v133
	v_fmac_f32_e32 v132, 0xba800000, v123
	v_pk_add_f32 v[134:135], v[44:45], v[44:45] op_sel_hi:[0,1]
	v_pk_mul_f32 v[44:45], v[132:133], v[132:133]
	v_pk_mul_f32 v[136:137], v[130:131], v[130:131]
	v_fmamk_f32 v40, v123, 0xba800000, v40
	v_pk_mov_b32 v[138:139], v[136:137], v[44:45] op_sel:[1,0]
	v_mov_b32_e32 v137, v45
	v_pk_add_f32 v[44:45], v[138:139], v[136:137]
	v_fmamk_f32 v41, v123, 0xba800000, v41
	v_pk_add_f32 v[136:137], v[44:45], v[44:45] op_sel_hi:[0,1]
	v_fmac_f32_e32 v42, 0xba800000, v123
	v_mul_f32_e32 v44, v40, v40
	v_fmamk_f32 v43, v123, 0xba800000, v43
	v_pk_fma_f32 v[138:139], v[40:41], v[40:41], v[44:45] op_sel_hi:[1,1,0]
	v_mul_f32_e32 v44, v42, v42
	v_pk_fma_f32 v[140:141], v[42:43], v[42:43], v[44:45] op_sel_hi:[1,1,0]
	v_fmamk_f32 v45, v123, 0xba800000, v37
	v_fmamk_f32 v44, v123, 0xba800000, v36
	v_fmamk_f32 v35, v123, 0xba800000, v35
	v_fmac_f32_e32 v34, 0xba800000, v123
	v_mul_f32_e32 v138, v34, v34
	v_mul_f32_e32 v140, v35, v35
	v_mul_f32_e32 v134, v44, v44
	v_mul_f32_e32 v136, v45, v45
	v_pk_add_f32 v[36:37], v[138:139], v[140:141]
	v_pk_add_f32 v[134:135], v[134:135], v[136:137]
	s_nop 0
	v_pk_add_f32 v[36:37], v[36:37], v[134:135]
	s_nop 0
	v_add_f32_e32 v123, v36, v37
	s_nop 1
	v_mov_b32_dpp v134, v123 quad_perm:[1,0,3,2] row_mask:0xf bank_mask:0xf
	v_pk_mul_f32 v[36:37], v[38:39], v[122:123] op_sel_hi:[1,0]
	v_pk_mul_f32 v[38:39], v[120:121], v[122:123] op_sel_hi:[1,0]
	s_waitcnt vmcnt(3)
	v_pk_fma_f32 v[36:37], v[10:11], v[36:37], v[14:15]
	v_pk_fma_f32 v[38:39], v[12:13], v[38:39], v[16:17]
	s_waitcnt lgkmcnt(0)
	v_add_f32_e32 v120, v123, v134
	s_nop 1
	v_mov_b32_dpp v121, v120 quad_perm:[2,3,0,1] row_mask:0xf bank_mask:0xf
	v_mul_f32_e32 v122, 0xbfb8aa3b, v36
	v_exp_f32_e32 v122, v122
	v_mul_f32_e32 v123, 0xbfb8aa3b, v37
	v_exp_f32_e32 v123, v123
	s_waitcnt lgkmcnt(0)
	v_add_f32_e32 v120, v120, v121
	s_nop 1
	v_mov_b32_dpp v121, v120 row_half_mirror row_mask:0xf bank_mask:0xf
	v_add_f32_e32 v122, 1.0, v122
	v_rcp_f32_e32 v122, v122
	v_add_f32_e32 v123, 1.0, v123
	v_rcp_f32_e32 v123, v123
	s_waitcnt lgkmcnt(0)
	v_add_f32_e32 v120, v120, v121
	s_nop 1
	v_mov_b32_dpp v121, v120 row_mirror row_mask:0xf bank_mask:0xf
	v_mul_f32_e32 v36, v36, v122
	v_mul_f32_e32 v122, 0xbfb8aa3b, v38
	v_exp_f32_e32 v122, v122
	v_mul_f32_e32 v37, v37, v123
	s_waitcnt lgkmcnt(0)
	v_add_f32_e32 v120, v120, v121
	ds_bpermute_b32 v121, v209, v120
	v_add_f32_e32 v122, 1.0, v122
	v_mul_f32_e32 v123, 0xbfb8aa3b, v39
	v_rcp_f32_e32 v122, v122
	v_exp_f32_e32 v123, v123
	s_waitcnt lgkmcnt(0)
	v_add_f32_e32 v120, v120, v121
	ds_bpermute_b32 v121, v210, v120
	v_cvt_pk_bf16_f32 v36, v36, v37
	v_mul_f32_e32 v37, v38, v122
	v_add_f32_e32 v38, 1.0, v123
	v_rcp_f32_e32 v38, v38
	s_waitcnt lgkmcnt(0)
	v_add_f32_e32 v120, v120, v121
	v_fmamk_f32 v120, v120, 0x3a800000, v211
	v_mul_f32_e32 v121, 0x4b800000, v120
	v_cmp_gt_f32_e32 vcc, s13, v120
	v_mul_f32_e32 v38, v39, v38
	v_cvt_pk_bf16_f32 v37, v37, v38
	global_store_dwordx2 v[124:125], v[36:37], off offset:1536
	v_cndmask_b32_e32 v120, v120, v121, vcc
	v_rsq_f32_e32 v120, v120
	v_lshl_add_u64 v[124:125], v[118:119], 0, s[6:7]
	s_sub_i32 s6, s0, 29
	s_ashr_i32 s7, s6, 31
	v_mul_f32_e32 v36, 0x45800000, v120
	v_cndmask_b32_e32 v122, v120, v36, vcc
	v_pk_mul_f32 v[36:37], v[126:127], v[122:123] op_sel_hi:[1,0]
	s_lshl_b64 s[6:7], s[6:7], 12
	v_pk_fma_f32 v[36:37], v[18:19], v[36:37], v[22:23]
	s_sub_i32 s0, s0, 28
	v_mul_f32_e32 v38, 0xbfb8aa3b, v36
	v_exp_f32_e32 v38, v38
	s_ashr_i32 s1, s0, 31
	s_lshl_b64 s[0:1], s[0:1], 12
	s_cmpk_lt_i32 s14, 0x200
	v_add_f32_e32 v38, 1.0, v38
	v_rcp_f32_e32 v120, v38
	v_mul_f32_e32 v38, 0xbfb8aa3b, v37
	v_exp_f32_e32 v121, v38
	v_pk_mul_f32 v[38:39], v[128:129], v[122:123] op_sel_hi:[1,0]
	v_mul_f32_e32 v36, v36, v120
	v_pk_fma_f32 v[38:39], v[20:21], v[38:39], v[24:25]
	v_add_f32_e32 v120, 1.0, v121
	v_mul_f32_e32 v121, 0xbfb8aa3b, v38
	v_mul_f32_e32 v123, 0xbfb8aa3b, v39
	v_exp_f32_e32 v121, v121
	v_exp_f32_e32 v123, v123
	v_rcp_f32_e32 v120, v120
	v_add_f32_e32 v121, 1.0, v121
	v_add_f32_e32 v123, 1.0, v123
	v_rcp_f32_e32 v121, v121
	v_rcp_f32_e32 v123, v123
	v_mul_f32_e32 v37, v37, v120
	v_cvt_pk_bf16_f32 v36, v36, v37
	v_mul_f32_e32 v37, v38, v121
	v_mul_f32_e32 v120, v39, v123
	v_pk_mul_f32 v[38:39], v[130:131], v[122:123] op_sel_hi:[1,0]
	v_cvt_pk_bf16_f32 v37, v37, v120
	global_store_dwordx2 v[124:125], v[36:37], off
	v_pk_fma_f32 v[38:39], v[2:3], v[38:39], v[6:7]
	s_nop 0
	v_mul_f32_e32 v121, 0xbfb8aa3b, v38
	v_exp_f32_e32 v121, v121
	s_nop 0
	v_add_f32_e32 v36, 1.0, v121
	v_rcp_f32_e32 v120, v36
	v_mul_f32_e32 v36, 0xbfb8aa3b, v39
	v_exp_f32_e32 v121, v36
	v_pk_mul_f32 v[36:37], v[132:133], v[122:123] op_sel_hi:[1,0]
	v_mul_f32_e32 v38, v38, v120
	v_pk_fma_f32 v[36:37], v[4:5], v[36:37], v[8:9]
	v_add_f32_e32 v120, 1.0, v121
	v_mul_f32_e32 v123, 0xbfb8aa3b, v37
	v_exp_f32_e32 v123, v123
	v_mul_f32_e32 v121, 0xbfb8aa3b, v36
	v_exp_f32_e32 v121, v121
	v_rcp_f32_e32 v120, v120
	v_add_f32_e32 v123, 1.0, v123
	v_rcp_f32_e32 v123, v123
	v_add_f32_e32 v121, 1.0, v121
	v_rcp_f32_e32 v121, v121
	v_mul_f32_e32 v39, v39, v120
	v_mul_f32_e32 v37, v37, v123
	v_add_u32_e32 v123, s10, v113
	ds_read_b128 v[126:129], v123
	ds_read_b128 v[130:133], v123 offset:1024
	v_mul_f32_e32 v36, v36, v121
	v_cvt_pk_bf16_f32 v38, v38, v39
	v_cvt_pk_bf16_f32 v39, v36, v37
	v_pk_mul_f32 v[36:37], v[40:41], v[122:123] op_sel_hi:[1,0]
	global_store_dwordx2 v[124:125], v[38:39], off offset:512
	v_pk_fma_f32 v[134:135], v[26:27], v[36:37], v[30:31]
	s_waitcnt lgkmcnt(1)
	v_mov_b32_e32 v36, v127
	v_mov_b32_e32 v37, v128
	v_mov_b32_e32 v38, v126
	v_mov_b32_e32 v39, v129
	v_pk_add_f32 v[36:37], v[36:37], v[38:39]
	v_pk_mul_f32 v[120:121], v[42:43], v[122:123] op_sel_hi:[1,0]
	v_add_f32_e32 v36, v36, v37
	v_add_f32_e32 v136, 0, v36
	ds_read_b128 v[40:43], v123 offset:2048
	ds_read_b128 v[36:39], v123 offset:3072
	s_waitcnt lgkmcnt(2)
	v_mov_b32_e32 v138, v131
	v_mov_b32_e32 v139, v132
	v_mov_b32_e32 v140, v130
	v_mov_b32_e32 v141, v133
	v_pk_add_f32 v[138:139], v[138:139], v[140:141]
	s_waitcnt lgkmcnt(1)
	v_add_f32_e32 v140, v40, v41
	v_pk_add_f32 v[138:139], v[138:139], v[138:139] op_sel:[0,1] op_sel_hi:[1,0]
	v_add_f32_e32 v142, v42, v43
	s_waitcnt lgkmcnt(0)
	v_mov_b32_e32 v137, v36
	v_mov_b32_e32 v139, v37
	v_mov_b32_e32 v141, v38
	v_mov_b32_e32 v143, v39
	v_pk_add_f32 v[136:137], v[136:137], v[138:139]
	v_pk_add_f32 v[138:139], v[140:141], v[142:143]
	v_pk_fma_f32 v[120:121], v[28:29], v[120:121], v[32:33]
	v_pk_add_f32 v[136:137], v[136:137], v[138:139]
	v_mul_f32_e32 v138, 0xbfb8aa3b, v135
	v_add_f32_e32 v123, v136, v137
	s_nop 1
	v_mov_b32_dpp v136, v123 quad_perm:[1,0,3,2] row_mask:0xf bank_mask:0xf
	v_mul_f32_e32 v137, 0xbfb8aa3b, v134
	v_exp_f32_e32 v137, v137
	v_exp_f32_e32 v138, v138
	s_waitcnt lgkmcnt(0)
	v_add_f32_e32 v123, v123, v136
	s_nop 1
	v_mov_b32_dpp v136, v123 quad_perm:[2,3,0,1] row_mask:0xf bank_mask:0xf
	v_add_f32_e32 v137, 1.0, v137
	v_add_f32_e32 v138, 1.0, v138
	v_rcp_f32_e32 v137, v137
	v_rcp_f32_e32 v138, v138
	s_waitcnt lgkmcnt(0)
	v_add_f32_e32 v123, v123, v136
	s_nop 1
	v_mov_b32_dpp v136, v123 row_half_mirror row_mask:0xf bank_mask:0xf
	v_mul_f32_e32 v134, v134, v137
	v_mul_f32_e32 v135, v135, v138
	v_cvt_pk_bf16_f32 v134, v134, v135
	v_mul_f32_e32 v137, 0xbfb8aa3b, v121
	s_waitcnt lgkmcnt(0)
	v_add_f32_e32 v123, v123, v136
	s_nop 1
	v_mov_b32_dpp v135, v123 row_mirror row_mask:0xf bank_mask:0xf
	v_mul_f32_e32 v136, 0xbfb8aa3b, v120
	v_exp_f32_e32 v136, v136
	v_exp_f32_e32 v137, v137
	s_waitcnt lgkmcnt(0)
	v_add_f32_e32 v123, v123, v135
	ds_bpermute_b32 v135, v209, v123
	v_add_f32_e32 v136, 1.0, v136
	v_add_f32_e32 v137, 1.0, v137
	v_rcp_f32_e32 v136, v136
	v_rcp_f32_e32 v137, v137
	s_waitcnt lgkmcnt(0)
	v_add_f32_e32 v123, v123, v135
	ds_bpermute_b32 v138, v210, v123
	v_mul_f32_e32 v120, v120, v136
	v_mul_f32_e32 v121, v121, v137
	v_cvt_pk_bf16_f32 v135, v120, v121
	global_store_dwordx2 v[124:125], v[134:135], off offset:1024
	s_waitcnt lgkmcnt(0)
	v_add_f32_e32 v123, v123, v138
	v_fmamk_f32 v127, v123, 0xba800000, v127
	v_fmamk_f32 v126, v123, 0xba800000, v126
	v_fmamk_f32 v129, v123, 0xba800000, v129
	v_fmac_f32_e32 v128, 0xba800000, v123
	v_pk_mul_f32 v[120:121], v[128:129], v[128:129]
	v_pk_mul_f32 v[134:135], v[126:127], v[126:127]
	v_fmamk_f32 v131, v123, 0xba800000, v131
	v_pk_mov_b32 v[136:137], v[134:135], v[120:121] op_sel:[1,0]
	v_mov_b32_e32 v135, v121
	v_pk_add_f32 v[120:121], v[136:137], v[134:135]
	v_fmamk_f32 v130, v123, 0xba800000, v130
	v_fmamk_f32 v133, v123, 0xba800000, v133
	v_fmac_f32_e32 v132, 0xba800000, v123
	v_pk_add_f32 v[134:135], v[120:121], v[120:121] op_sel_hi:[0,1]
	v_pk_mul_f32 v[120:121], v[132:133], v[132:133]
	v_pk_mul_f32 v[136:137], v[130:131], v[130:131]
	v_fmamk_f32 v40, v123, 0xba800000, v40
	v_pk_mov_b32 v[138:139], v[136:137], v[120:121] op_sel:[1,0]
	v_mov_b32_e32 v137, v121
	v_pk_add_f32 v[120:121], v[138:139], v[136:137]
	v_fmamk_f32 v41, v123, 0xba800000, v41
	v_pk_add_f32 v[136:137], v[120:121], v[120:121] op_sel_hi:[0,1]
	v_fmac_f32_e32 v42, 0xba800000, v123
	v_mul_f32_e32 v120, v40, v40
	v_fmamk_f32 v43, v123, 0xba800000, v43
	v_pk_fma_f32 v[138:139], v[40:41], v[40:41], v[120:121] op_sel_hi:[1,1,0]
	v_mul_f32_e32 v120, v42, v42
	v_pk_fma_f32 v[140:141], v[42:43], v[42:43], v[120:121] op_sel_hi:[1,1,0]
	v_fmamk_f32 v121, v123, 0xba800000, v39
	v_fmamk_f32 v120, v123, 0xba800000, v38
	v_fmamk_f32 v37, v123, 0xba800000, v37
	v_fmac_f32_e32 v36, 0xba800000, v123
	v_mul_f32_e32 v138, v36, v36
	v_mul_f32_e32 v140, v37, v37
	v_mul_f32_e32 v134, v120, v120
	v_mul_f32_e32 v136, v121, v121
	v_pk_add_f32 v[38:39], v[138:139], v[140:141]
	v_pk_add_f32 v[134:135], v[134:135], v[136:137]
	s_nop 0
	v_pk_add_f32 v[38:39], v[38:39], v[134:135]
	s_nop 0
	v_add_f32_e32 v123, v38, v39
	s_nop 1
	v_mov_b32_dpp v134, v123 quad_perm:[1,0,3,2] row_mask:0xf bank_mask:0xf
	v_pk_mul_f32 v[38:39], v[44:45], v[122:123] op_sel_hi:[1,0]
	v_pk_mul_f32 v[34:35], v[34:35], v[122:123] op_sel_hi:[1,0]
	v_pk_fma_f32 v[38:39], v[12:13], v[38:39], v[16:17]
	v_pk_fma_f32 v[34:35], v[10:11], v[34:35], v[14:15]
	s_waitcnt lgkmcnt(0)
	v_add_f32_e32 v44, v123, v134
	s_nop 1
	v_mov_b32_dpp v45, v44 quad_perm:[2,3,0,1] row_mask:0xf bank_mask:0xf
	v_mul_f32_e32 v122, 0xbfb8aa3b, v34
	v_exp_f32_e32 v122, v122
	v_mul_f32_e32 v123, 0xbfb8aa3b, v35
	v_exp_f32_e32 v123, v123
	s_waitcnt lgkmcnt(0)
	v_add_f32_e32 v44, v44, v45
	s_nop 1
	v_mov_b32_dpp v45, v44 row_half_mirror row_mask:0xf bank_mask:0xf
	v_add_f32_e32 v122, 1.0, v122
	v_rcp_f32_e32 v122, v122
	v_add_f32_e32 v123, 1.0, v123
	v_rcp_f32_e32 v123, v123
	s_waitcnt lgkmcnt(0)
	v_add_f32_e32 v44, v44, v45
	s_nop 1
	v_mov_b32_dpp v45, v44 row_mirror row_mask:0xf bank_mask:0xf
	v_mul_f32_e32 v34, v34, v122
	v_mul_f32_e32 v122, 0xbfb8aa3b, v38
	v_exp_f32_e32 v122, v122
	v_mul_f32_e32 v35, v35, v123
	s_waitcnt lgkmcnt(0)
	v_add_f32_e32 v44, v44, v45
	ds_bpermute_b32 v45, v209, v44
	v_add_f32_e32 v122, 1.0, v122
	v_mul_f32_e32 v123, 0xbfb8aa3b, v39
	v_rcp_f32_e32 v122, v122
	v_exp_f32_e32 v123, v123
	s_waitcnt lgkmcnt(0)
	v_add_f32_e32 v44, v44, v45
	ds_bpermute_b32 v45, v210, v44
	v_cvt_pk_bf16_f32 v34, v34, v35
	v_mul_f32_e32 v35, v38, v122
	v_add_f32_e32 v38, 1.0, v123
	v_rcp_f32_e32 v38, v38
	s_waitcnt lgkmcnt(0)
	v_add_f32_e32 v44, v44, v45
	v_fmamk_f32 v44, v44, 0x3a800000, v211
	v_mul_f32_e32 v45, 0x4b800000, v44
	v_cmp_gt_f32_e32 vcc, s13, v44
	v_mul_f32_e32 v38, v39, v38
	v_cvt_pk_bf16_f32 v35, v35, v38
	global_store_dwordx2 v[124:125], v[34:35], off offset:1536
	v_cndmask_b32_e32 v44, v44, v45, vcc
	v_rsq_f32_e32 v44, v44
	s_nop 0
	v_mul_f32_e32 v34, 0x45800000, v44
	v_cndmask_b32_e32 v34, v44, v34, vcc
	v_pk_mul_f32 v[38:39], v[126:127], v[34:35] op_sel_hi:[1,0]
	s_nop 0
	v_pk_fma_f32 v[38:39], v[18:19], v[38:39], v[22:23]
	s_nop 0
	v_mul_f32_e32 v35, 0xbfb8aa3b, v38
	v_exp_f32_e32 v35, v35
	v_mul_f32_e32 v44, 0xbfb8aa3b, v39
	v_exp_f32_e32 v122, v44
	v_add_f32_e32 v35, 1.0, v35
	v_rcp_f32_e32 v35, v35
	s_nop 0
	v_pk_mul_f32 v[44:45], v[128:129], v[34:35] op_sel_hi:[1,0]
	s_nop 0
	v_pk_fma_f32 v[44:45], v[20:21], v[44:45], v[24:25]
	v_mul_f32_e32 v35, v38, v35
	v_add_f32_e32 v38, 1.0, v122
	v_mul_f32_e32 v122, 0xbfb8aa3b, v44
	v_exp_f32_e32 v122, v122
	v_mul_f32_e32 v123, 0xbfb8aa3b, v45
	v_exp_f32_e32 v123, v123
	v_rcp_f32_e32 v38, v38
	v_add_f32_e32 v122, 1.0, v122
	v_rcp_f32_e32 v122, v122
	v_add_f32_e32 v123, 1.0, v123
	v_rcp_f32_e32 v123, v123
	v_mul_f32_e32 v38, v39, v38
	v_cvt_pk_bf16_f32 v38, v35, v38
	v_mul_f32_e32 v35, v44, v122
	v_mul_f32_e32 v39, v45, v123
	v_pk_mul_f32 v[44:45], v[130:131], v[34:35] op_sel_hi:[1,0]
	v_cvt_pk_bf16_f32 v39, v35, v39
	s_nop 0
	v_pk_fma_f32 v[44:45], v[2:3], v[44:45], v[6:7]
	s_nop 0
	v_mul_f32_e32 v122, 0xbfb8aa3b, v44
	v_exp_f32_e32 v124, v122
	v_lshl_add_u64 v[122:123], v[118:119], 0, s[6:7]
	global_store_dwordx2 v[122:123], v[38:39], off
	v_mul_f32_e32 v38, 0xbfb8aa3b, v45
	v_add_f32_e32 v35, 1.0, v124
	v_rcp_f32_e32 v35, v35
	v_exp_f32_e32 v124, v38
	v_pk_mul_f32 v[38:39], v[132:133], v[34:35] op_sel_hi:[1,0]
	s_nop 0
	v_pk_fma_f32 v[38:39], v[4:5], v[38:39], v[8:9]
	v_mul_f32_e32 v35, v44, v35
	v_add_f32_e32 v44, 1.0, v124
	v_mul_f32_e32 v124, 0xbfb8aa3b, v38
	v_exp_f32_e32 v124, v124
	v_mul_f32_e32 v125, 0xbfb8aa3b, v39
	v_exp_f32_e32 v125, v125
	v_rcp_f32_e32 v44, v44
	v_add_f32_e32 v124, 1.0, v124
	v_rcp_f32_e32 v124, v124
	v_add_f32_e32 v125, 1.0, v125
	v_rcp_f32_e32 v125, v125
	v_mul_f32_e32 v44, v45, v44
	v_cvt_pk_bf16_f32 v44, v35, v44
	v_mul_f32_e32 v35, v38, v124
	v_mul_f32_e32 v38, v39, v125
	v_cvt_pk_bf16_f32 v45, v35, v38
	v_add_u32_e32 v35, s11, v113
	ds_read_b128 v[124:127], v35
	ds_read_b128 v[128:131], v35 offset:1024
	v_pk_mul_f32 v[38:39], v[40:41], v[34:35] op_sel_hi:[1,0]
	global_store_dwordx2 v[122:123], v[44:45], off offset:512
	v_pk_fma_f32 v[134:135], v[26:27], v[38:39], v[30:31]
	s_waitcnt lgkmcnt(1)
	v_mov_b32_e32 v38, v125
	v_mov_b32_e32 v39, v126
	v_mov_b32_e32 v40, v124
	v_mov_b32_e32 v41, v127
	v_pk_add_f32 v[38:39], v[38:39], v[40:41]
	v_pk_mul_f32 v[132:133], v[42:43], v[34:35] op_sel_hi:[1,0]
	v_add_f32_e32 v38, v38, v39
	v_add_f32_e32 v136, 0, v38
	ds_read_b128 v[42:45], v35 offset:2048
	ds_read_b128 v[38:41], v35 offset:3072
	s_waitcnt lgkmcnt(2)
	v_mov_b32_e32 v138, v129
	v_mov_b32_e32 v139, v130
	v_mov_b32_e32 v140, v128
	v_mov_b32_e32 v141, v131
	v_pk_add_f32 v[138:139], v[138:139], v[140:141]
	s_waitcnt lgkmcnt(1)
	v_add_f32_e32 v140, v42, v43
	v_pk_add_f32 v[138:139], v[138:139], v[138:139] op_sel:[0,1] op_sel_hi:[1,0]
	v_add_f32_e32 v142, v44, v45
	s_waitcnt lgkmcnt(0)
	v_mov_b32_e32 v137, v38
	v_mov_b32_e32 v139, v39
	v_mov_b32_e32 v141, v40
	v_mov_b32_e32 v143, v41
	v_pk_add_f32 v[136:137], v[136:137], v[138:139]
	v_pk_add_f32 v[138:139], v[140:141], v[142:143]
	v_pk_fma_f32 v[132:133], v[28:29], v[132:133], v[32:33]
	v_pk_add_f32 v[136:137], v[136:137], v[138:139]
	v_mul_f32_e32 v138, 0xbfb8aa3b, v135
	v_add_f32_e32 v35, v136, v137
	s_nop 1
	v_mov_b32_dpp v136, v35 quad_perm:[1,0,3,2] row_mask:0xf bank_mask:0xf
	v_mul_f32_e32 v137, 0xbfb8aa3b, v134
	v_exp_f32_e32 v137, v137
	v_exp_f32_e32 v138, v138
	s_waitcnt lgkmcnt(0)
	v_add_f32_e32 v35, v35, v136
	s_nop 1
	v_mov_b32_dpp v136, v35 quad_perm:[2,3,0,1] row_mask:0xf bank_mask:0xf
	v_add_f32_e32 v137, 1.0, v137
	v_add_f32_e32 v138, 1.0, v138
	v_rcp_f32_e32 v137, v137
	v_rcp_f32_e32 v138, v138
	s_waitcnt lgkmcnt(0)
	v_add_f32_e32 v35, v35, v136
	s_nop 1
	v_mov_b32_dpp v136, v35 row_half_mirror row_mask:0xf bank_mask:0xf
	v_mul_f32_e32 v134, v134, v137
	v_mul_f32_e32 v135, v135, v138
	v_cvt_pk_bf16_f32 v134, v134, v135
	v_mul_f32_e32 v137, 0xbfb8aa3b, v133
	s_waitcnt lgkmcnt(0)
	v_add_f32_e32 v35, v35, v136
	s_nop 1
	v_mov_b32_dpp v135, v35 row_mirror row_mask:0xf bank_mask:0xf
	v_mul_f32_e32 v136, 0xbfb8aa3b, v132
	v_exp_f32_e32 v136, v136
	v_exp_f32_e32 v137, v137
	s_waitcnt lgkmcnt(0)
	v_add_f32_e32 v35, v35, v135
	ds_bpermute_b32 v135, v209, v35
	v_add_f32_e32 v136, 1.0, v136
	v_add_f32_e32 v137, 1.0, v137
	v_rcp_f32_e32 v136, v136
	v_rcp_f32_e32 v137, v137
	s_waitcnt lgkmcnt(0)
	v_add_f32_e32 v35, v35, v135
	ds_bpermute_b32 v138, v210, v35
	v_mul_f32_e32 v132, v132, v136
	v_mul_f32_e32 v133, v133, v137
	v_cvt_pk_bf16_f32 v135, v132, v133
	global_store_dwordx2 v[122:123], v[134:135], off offset:1024
	s_waitcnt lgkmcnt(0)
	v_add_f32_e32 v35, v35, v138
	v_fmamk_f32 v125, v35, 0xba800000, v125
	v_fmamk_f32 v124, v35, 0xba800000, v124
	v_fmamk_f32 v127, v35, 0xba800000, v127
	v_fmac_f32_e32 v126, 0xba800000, v35
	v_pk_mul_f32 v[132:133], v[126:127], v[126:127]
	v_pk_mul_f32 v[134:135], v[124:125], v[124:125]
	v_fmamk_f32 v129, v35, 0xba800000, v129
	v_pk_mov_b32 v[136:137], v[134:135], v[132:133] op_sel:[1,0]
	v_mov_b32_e32 v135, v133
	v_pk_add_f32 v[132:133], v[136:137], v[134:135]
	v_fmamk_f32 v128, v35, 0xba800000, v128
	v_fmamk_f32 v131, v35, 0xba800000, v131
	v_fmac_f32_e32 v130, 0xba800000, v35
	v_pk_add_f32 v[132:133], v[132:133], v[132:133] op_sel_hi:[0,1]
	v_pk_mul_f32 v[134:135], v[130:131], v[130:131]
	v_pk_mul_f32 v[136:137], v[128:129], v[128:129]
	v_fmamk_f32 v42, v35, 0xba800000, v42
	v_pk_mov_b32 v[138:139], v[136:137], v[134:135] op_sel:[1,0]
	v_mov_b32_e32 v137, v135
	v_fmamk_f32 v43, v35, 0xba800000, v43
	v_fmac_f32_e32 v44, 0xba800000, v35
	v_mul_f32_e32 v132, v42, v42
	v_pk_add_f32 v[134:135], v[138:139], v[136:137]
	v_fmamk_f32 v45, v35, 0xba800000, v45
	v_pk_fma_f32 v[136:137], v[42:43], v[42:43], v[132:133] op_sel_hi:[1,1,0]
	v_mul_f32_e32 v132, v44, v44
	v_pk_add_f32 v[134:135], v[134:135], v[134:135] op_sel_hi:[0,1]
	v_pk_fma_f32 v[138:139], v[44:45], v[44:45], v[132:133] op_sel_hi:[1,1,0]
	v_fmamk_f32 v41, v35, 0xba800000, v41
	v_fmamk_f32 v40, v35, 0xba800000, v40
	v_fmamk_f32 v39, v35, 0xba800000, v39
	v_fmac_f32_e32 v38, 0xba800000, v35
	v_mul_f32_e32 v136, v38, v38
	v_mul_f32_e32 v138, v39, v39
	v_mul_f32_e32 v132, v40, v40
	v_mul_f32_e32 v134, v41, v41
	v_pk_add_f32 v[136:137], v[136:137], v[138:139]
	v_pk_add_f32 v[132:133], v[132:133], v[134:135]
	v_pk_mul_f32 v[36:37], v[36:37], v[34:35] op_sel_hi:[1,0]
	v_pk_add_f32 v[132:133], v[136:137], v[132:133]
	v_pk_mul_f32 v[34:35], v[120:121], v[34:35] op_sel_hi:[1,0]
	v_add_f32_e32 v132, v132, v133
	s_nop 1
	v_mov_b32_dpp v133, v132 quad_perm:[1,0,3,2] row_mask:0xf bank_mask:0xf
	v_pk_fma_f32 v[36:37], v[10:11], v[36:37], v[14:15]
	v_pk_fma_f32 v[34:35], v[12:13], v[34:35], v[16:17]
	s_waitcnt lgkmcnt(0)
	v_add_f32_e32 v120, v132, v133
	s_nop 1
	v_mov_b32_dpp v121, v120 quad_perm:[2,3,0,1] row_mask:0xf bank_mask:0xf
	v_mul_f32_e32 v132, 0xbfb8aa3b, v36
	v_exp_f32_e32 v132, v132
	v_mul_f32_e32 v133, 0xbfb8aa3b, v37
	v_exp_f32_e32 v133, v133
	s_waitcnt lgkmcnt(0)
	v_add_f32_e32 v120, v120, v121
	s_nop 1
	v_mov_b32_dpp v121, v120 row_half_mirror row_mask:0xf bank_mask:0xf
	v_add_f32_e32 v132, 1.0, v132
	v_rcp_f32_e32 v132, v132
	v_add_f32_e32 v133, 1.0, v133
	v_rcp_f32_e32 v133, v133
	s_waitcnt lgkmcnt(0)
	v_add_f32_e32 v120, v120, v121
	s_nop 1
	v_mov_b32_dpp v121, v120 row_mirror row_mask:0xf bank_mask:0xf
	v_mul_f32_e32 v36, v36, v132
	v_mul_f32_e32 v132, 0xbfb8aa3b, v34
	v_exp_f32_e32 v132, v132
	v_mul_f32_e32 v37, v37, v133
	s_waitcnt lgkmcnt(0)
	v_add_f32_e32 v120, v120, v121
	ds_bpermute_b32 v121, v209, v120
	v_mul_f32_e32 v133, 0xbfb8aa3b, v35
	v_exp_f32_e32 v133, v133
	v_add_f32_e32 v132, 1.0, v132
	v_rcp_f32_e32 v132, v132
	s_waitcnt lgkmcnt(0)
	v_add_f32_e32 v120, v120, v121
	ds_bpermute_b32 v121, v210, v120
	v_cvt_pk_bf16_f32 v36, v36, v37
	v_add_f32_e32 v37, 1.0, v133
	v_rcp_f32_e32 v37, v37
	v_mul_f32_e32 v34, v34, v132
	s_waitcnt lgkmcnt(0)
	v_add_f32_e32 v120, v120, v121
	v_fmamk_f32 v120, v120, 0x3a800000, v211
	v_mul_f32_e32 v121, 0x4b800000, v120
	v_cmp_gt_f32_e32 vcc, s13, v120
	v_mul_f32_e32 v35, v35, v37
	v_cvt_pk_bf16_f32 v37, v34, v35
	global_store_dwordx2 v[122:123], v[36:37], off offset:1536
	v_cndmask_b32_e32 v120, v120, v121, vcc
	v_rsq_f32_e32 v120, v120
	s_nop 0
	v_mul_f32_e32 v34, 0x45800000, v120
	v_cndmask_b32_e32 v34, v120, v34, vcc
	v_pk_mul_f32 v[36:37], v[124:125], v[34:35] op_sel_hi:[1,0]
	s_nop 0
	v_pk_fma_f32 v[18:19], v[18:19], v[36:37], v[22:23]
	s_nop 0
	v_mul_f32_e32 v22, 0xbfb8aa3b, v18
	v_exp_f32_e32 v22, v22
	s_nop 0
	v_add_f32_e32 v22, 1.0, v22
	v_rcp_f32_e32 v35, v22
	v_mul_f32_e32 v22, 0xbfb8aa3b, v19
	v_exp_f32_e32 v36, v22
	v_pk_mul_f32 v[22:23], v[126:127], v[34:35] op_sel_hi:[1,0]
	s_nop 0
	v_pk_fma_f32 v[20:21], v[20:21], v[22:23], v[24:25]
	v_add_f32_e32 v22, 1.0, v36
	v_mul_f32_e32 v23, 0xbfb8aa3b, v20
	v_mul_f32_e32 v24, 0xbfb8aa3b, v21
	v_exp_f32_e32 v23, v23
	v_exp_f32_e32 v24, v24
	v_rcp_f32_e32 v22, v22
	v_mul_f32_e32 v18, v18, v35
	v_add_f32_e32 v23, 1.0, v23
	v_add_f32_e32 v24, 1.0, v24
	v_rcp_f32_e32 v23, v23
	v_rcp_f32_e32 v24, v24
	v_mul_f32_e32 v19, v19, v22
	v_cvt_pk_bf16_f32 v18, v18, v19
	v_mul_f32_e32 v19, v20, v23
	v_mul_f32_e32 v22, v21, v24
	v_pk_mul_f32 v[20:21], v[128:129], v[34:35] op_sel_hi:[1,0]
	v_cvt_pk_bf16_f32 v19, v19, v22
	s_nop 0
	v_pk_fma_f32 v[2:3], v[2:3], v[20:21], v[6:7]
	s_nop 0
	v_mul_f32_e32 v6, 0xbfb8aa3b, v2
	v_exp_f32_e32 v20, v6
	v_lshl_add_u64 v[6:7], v[118:119], 0, s[0:1]
	global_store_dwordx2 v[6:7], v[18:19], off
	v_add_f32_e32 v18, 1.0, v20
	v_rcp_f32_e32 v20, v18
	v_mul_f32_e32 v18, 0xbfb8aa3b, v3
	v_exp_f32_e32 v21, v18
	v_pk_mul_f32 v[18:19], v[130:131], v[34:35] op_sel_hi:[1,0]
	v_mul_f32_e32 v2, v2, v20
	v_pk_fma_f32 v[4:5], v[4:5], v[18:19], v[8:9]
	v_add_f32_e32 v8, 1.0, v21
	v_mul_f32_e32 v9, 0xbfb8aa3b, v4
	v_mul_f32_e32 v18, 0xbfb8aa3b, v5
	v_exp_f32_e32 v9, v9
	v_exp_f32_e32 v18, v18
	v_rcp_f32_e32 v8, v8
	v_add_f32_e32 v9, 1.0, v9
	v_add_f32_e32 v18, 1.0, v18
	v_rcp_f32_e32 v9, v9
	v_rcp_f32_e32 v18, v18
	v_mul_f32_e32 v3, v3, v8
	v_cvt_pk_bf16_f32 v2, v2, v3
	v_mul_f32_e32 v3, v4, v9
	v_mul_f32_e32 v4, v5, v18
	v_cvt_pk_bf16_f32 v3, v3, v4
	v_pk_mul_f32 v[4:5], v[42:43], v[34:35] op_sel_hi:[1,0]
	global_store_dwordx2 v[6:7], v[2:3], off offset:512
	v_pk_fma_f32 v[4:5], v[26:27], v[4:5], v[30:31]
	v_pk_mul_f32 v[2:3], v[44:45], v[34:35] op_sel_hi:[1,0]
	v_mul_f32_e32 v8, 0xbfb8aa3b, v4
	v_exp_f32_e32 v8, v8
	v_pk_fma_f32 v[2:3], v[28:29], v[2:3], v[32:33]
	v_mul_f32_e32 v9, 0xbfb8aa3b, v5
	v_mul_f32_e32 v18, 0xbfb8aa3b, v2
	v_add_f32_e32 v8, 1.0, v8
	v_rcp_f32_e32 v8, v8
	v_exp_f32_e32 v9, v9
	v_exp_f32_e32 v18, v18
	v_mul_f32_e32 v4, v4, v8
	v_add_f32_e32 v8, 1.0, v9
	v_add_f32_e32 v9, 1.0, v18
	v_rcp_f32_e32 v8, v8
	v_rcp_f32_e32 v9, v9
	v_mul_f32_e32 v18, 0xbfb8aa3b, v3
	v_exp_f32_e32 v18, v18
	v_mul_f32_e32 v5, v5, v8
	v_mul_f32_e32 v2, v2, v9
	v_pk_mul_f32 v[8:9], v[38:39], v[34:35] op_sel_hi:[1,0]
	v_cvt_pk_bf16_f32 v4, v4, v5
	v_add_f32_e32 v5, 1.0, v18
	v_pk_fma_f32 v[8:9], v[10:11], v[8:9], v[14:15]
	v_rcp_f32_e32 v5, v5
	v_mul_f32_e32 v10, 0xbfb8aa3b, v8
	v_exp_f32_e32 v10, v10
	v_mul_f32_e32 v3, v3, v5
	v_cvt_pk_bf16_f32 v5, v2, v3
	v_add_f32_e32 v2, 1.0, v10
	global_store_dwordx2 v[6:7], v[4:5], off offset:1024
	v_rcp_f32_e32 v4, v2
	v_mul_f32_e32 v2, 0xbfb8aa3b, v9
	v_exp_f32_e32 v5, v2
	v_pk_mul_f32 v[2:3], v[40:41], v[34:35] op_sel_hi:[1,0]
	v_mul_f32_e32 v4, v8, v4
	v_pk_fma_f32 v[2:3], v[12:13], v[2:3], v[16:17]
	v_add_f32_e32 v5, 1.0, v5
	v_mul_f32_e32 v8, 0xbfb8aa3b, v2
	v_mul_f32_e32 v10, 0xbfb8aa3b, v3
	v_exp_f32_e32 v8, v8
	v_exp_f32_e32 v10, v10
	v_rcp_f32_e32 v5, v5
	v_add_f32_e32 v8, 1.0, v8
	v_add_f32_e32 v10, 1.0, v10
	v_rcp_f32_e32 v8, v8
	v_rcp_f32_e32 v10, v10
	v_mul_f32_e32 v5, v9, v5
	v_cvt_pk_bf16_f32 v4, v4, v5
	v_mul_f32_e32 v2, v2, v8
	v_mul_f32_e32 v3, v3, v10
	v_cvt_pk_bf16_f32 v5, v2, v3
	global_store_dwordx2 v[6:7], v[4:5], off offset:1536
	s_cbranch_scc0 .LBB0_408
